# first K-loop trip peeled (C=0) instead of explicit accumulator clears
# speedup vs baseline: 1.0084x; 1.0084x over previous
; template <class Epi, class Sched, class Prob>
; __device__ __forceinline__ void gemm_phase(LAS unsigned char* lds, LAS unsigned char* lds_epi, const Prob g, const Sched& S, const Epi& E, int wid) {
;     ...
;     Unit cur, nxt; int ui = 0; int epi_pm = -1;
;     if (!S.next(0, cur)) return;
;     const int Ra0 = aperm_of<Epi>::v ? perm_a64(R0) : R0, Ra1 = aperm_of<Epi>::v ? perm_a64(R1) : R1;
;     const unsigned cA00 = (unsigned)Ra0 * lda2 + (unsigned)C0 * 2u, cA01 = (unsigned)Ra1 * lda2 + (unsigned)C1 * 2u, cA10 = cA00 + (unsigned)HALF * lda2, cA11 = cA01 + (unsigned)HALF * lda2;
;     f32x4 acc[2][2][4][2];
;     ...
;     PG8_ACC_INIT(cur);
;     bf16x8 At[4][2], B0[2][2], B1[2][2];
;     const char* cA = g.a_base(cur); const char* cB = g.b_base(cur);
;     PG8_STAGE(PG8_SB(0, 0), cB, vB0, vB1); PG8_STAGE(PG8_SB(0, 1), cB + hstepB, vB0, vB1); PG8_STAGE(PG8_SA(0, 0), cA, cA00, cA01); PG8_STAGE(PG8_SA(0, 1), cA, cA10, cA11);
;     if (wr == 1) PG8_BAR;
;     PG8_WAIT_V(2); PG8_BAR;
;     PG8_STAGE(PG8_SB(1, 0), cB + kstep, vB0, vB1); PG8_STAGE(PG8_SA(1, 0), cA + kstep, cA00, cA01); PG8_STAGE(PG8_SB(1, 1), cB + hstepB + kstep, vB0, vB1);
;     PG8_WAIT_V(6); PG8_BAR;
;     for (;;) {
;         const bool has_next = S.next(ui + 1, nxt);
;         const char* nA = has_next ? g.a_base(nxt) : cA; const char* nB = has_next ? g.b_base(nxt) : cB;
; _Pragma("clang loop unroll(disable)")
;         for (int t = 0; t < nt; t += 2) {
;             const bool last = (t == nt - 2);
;             const char* a1 = cA + (size_t)(t + 1) * kstep;
;             const char* a2 = last ? nA : cA + (size_t)(t + 2) * kstep; const char* b2 = last ? nB : cB + (size_t)(t + 2) * kstep;
;             const char* a3 = a2 + kstep; const char* b3 = b2 + kstep;
;             PG8_LDB(B0, 0, 0); PG8_LDB(B1, 0, 1); PG8_SCHED; PG8_LDA(At, 0, 0); PG8_STAGE(PG8_SA(1, 1), a1, cA10, cA11);
;             PG8_WAIT_V(8); PG8_WAIT_L(0); PG8_BAR; PG8_MMA(0, 0, At, B0); PG8_MMA(0, 1, At, B1); PG8_BAR; PG8_SCHED;
;             PG8_LDA(At, 0, 1); PG8_STAGE(PG8_SB(0, 0), b2, vB0, vB1); PG8_STAGE(PG8_SB(0, 1), b2 + hstepB, vB0, vB1); PG8_STAGE(PG8_SA(0, 0), a2, cA00, cA01);
;             PG8_WAIT_V(8); PG8_WAIT_L(0); PG8_BAR; PG8_MMA(1, 0, At, B0); PG8_MMA(1, 1, At, B1); PG8_BAR; PG8_SCHED;
;             PG8_LDB(B0, 1, 0); PG8_LDB(B1, 1, 1); PG8_SCHED; PG8_LDA(At, 1, 0); PG8_STAGE(PG8_SA(0, 1), a2, cA10, cA11);
.LBB0_261:
	s_ashr_i32 s3, s2, 31
	s_lshl_b64 s[48:49], s[2:3], 20
	s_add_u32 s48, s33, s48
	s_addc_u32 s49, s39, s49
	s_and_b64 s[50:51], s[46:47], exec
	s_cselect_b32 s3, s49, s15
	s_cselect_b32 s77, s48, s14
	s_ashr_i32 s45, s44, 31
	s_lshl_b64 s[50:51], s[44:45], 20
	s_add_u32 s50, s56, s50
	s_addc_u32 s51, s57, s51
	s_and_b64 s[54:55], s[46:47], exec
	s_cselect_b32 s45, s51, s53
	s_cselect_b32 s78, s50, s52
	s_add_u32 s14, s14, 0x80
	s_addc_u32 s15, s15, 0
	s_add_u32 s79, s52, 0x100
	v_mov_b32_e32 v44, 0
	s_addc_u32 s80, s53, 0
	s_mov_b32 s81, -2
	v_add_u32_e32 v140, s72, v194
	v_add_u32_e32 v156, s73, v194
	ds_read_b128 v[128:131], v140
	ds_read_b128 v[132:135], v140 offset:1024
	ds_read_b128 v[136:139], v140 offset:2048
	ds_read_b128 v[140:143], v140 offset:3072
	ds_read_b128 v[174:177], v156
	ds_read_b128 v[178:181], v156 offset:1024
	ds_read_b128 v[182:185], v156 offset:2048
	ds_read_b128 v[186:189], v156 offset:3072
	s_add_u32 s52, s14, 0x80
	s_addc_u32 s53, s15, 0
	s_cmp_eq_u32 s81, 28
	s_cselect_b32 s55, s3, s53
	s_cselect_b32 s54, s77, s52
	s_cselect_b32 s53, s45, s80
	s_cselect_b32 s52, s78, s79
	v_lshl_add_u64 v[190:191], s[14:15], 0, v[170:171]
	s_add_i32 m0, s25, 0xc000
	ds_read_b128 v[208:211], v204
	ds_read_b128 v[212:215], v204 offset:1024
	ds_read_b128 v[216:219], v204 offset:2048
	ds_read_b128 v[220:223], v204 offset:3072
	ds_read_b128 v[224:227], v204 offset:4096
	ds_read_b128 v[228:231], v204 offset:5120
	ds_read_b128 v[232:235], v204 offset:6144
	ds_read_b128 v[238:241], v204 offset:7168
	global_load_lds_dwordx4 v[190:191], off
	v_lshl_add_u64 v[190:191], s[14:15], 0, v[168:169]
	s_add_i32 m0, s25, 0xe000
	s_nop 0
	global_load_lds_dwordx4 v[190:191], off
	s_waitcnt vmcnt(8)
	s_waitcnt lgkmcnt(0)
	s_barrier
	s_setprio 1
	s_waitcnt lgkmcnt(0)
	v_mfma_f32_16x16x32_bf16 v[80:83], v[128:131], v[208:211], 0
	v_mfma_f32_16x16x32_bf16 v[92:95], v[136:139], v[208:211], 0
	v_mfma_f32_16x16x32_bf16 v[52:55], v[128:131], v[216:219], 0
	v_mfma_f32_16x16x32_bf16 v[68:71], v[136:139], v[216:219], 0
	v_mfma_f32_16x16x32_bf16 v[28:31], v[128:131], v[224:227], 0
	v_mfma_f32_16x16x32_bf16 v[36:39], v[136:139], v[224:227], 0
	v_mfma_f32_16x16x32_bf16 v[8:11], v[128:131], v[232:235], 0
	v_mfma_f32_16x16x32_bf16 v[16:19], v[136:139], v[232:235], 0
	v_mfma_f32_16x16x32_bf16 v[80:83], v[132:135], v[212:215], v[80:83]
	v_mfma_f32_16x16x32_bf16 v[92:95], v[140:143], v[212:215], v[92:95]
	v_mfma_f32_16x16x32_bf16 v[52:55], v[132:135], v[220:223], v[52:55]
	v_mfma_f32_16x16x32_bf16 v[68:71], v[140:143], v[220:223], v[68:71]
	v_mfma_f32_16x16x32_bf16 v[28:31], v[132:135], v[228:231], v[28:31]
	v_mfma_f32_16x16x32_bf16 v[36:39], v[140:143], v[228:231], v[36:39]
	v_mfma_f32_16x16x32_bf16 v[8:11], v[132:135], v[238:241], v[8:11]
	v_mfma_f32_16x16x32_bf16 v[16:19], v[140:143], v[238:241], v[16:19]
	s_setprio 0
	s_setprio 1
	v_mfma_f32_16x16x32_bf16 v[120:123], v[174:177], v[208:211], 0
	v_mfma_f32_16x16x32_bf16 v[124:127], v[182:185], v[208:211], 0
	v_mfma_f32_16x16x32_bf16 v[104:107], v[174:177], v[216:219], 0
	v_mfma_f32_16x16x32_bf16 v[112:115], v[182:185], v[216:219], 0
	v_mfma_f32_16x16x32_bf16 v[84:87], v[174:177], v[224:227], 0
	v_mfma_f32_16x16x32_bf16 v[96:99], v[182:185], v[224:227], 0
	v_mfma_f32_16x16x32_bf16 v[48:51], v[174:177], v[232:235], 0
	v_mfma_f32_16x16x32_bf16 v[64:67], v[182:185], v[232:235], 0
	v_mfma_f32_16x16x32_bf16 v[120:123], v[178:181], v[212:215], v[120:123]
	v_mfma_f32_16x16x32_bf16 v[124:127], v[186:189], v[212:215], v[124:127]
	v_mfma_f32_16x16x32_bf16 v[104:107], v[178:181], v[220:223], v[104:107]
	v_mfma_f32_16x16x32_bf16 v[112:115], v[186:189], v[220:223], v[112:115]
	v_mfma_f32_16x16x32_bf16 v[84:87], v[178:181], v[228:231], v[84:87]
	v_mfma_f32_16x16x32_bf16 v[96:99], v[186:189], v[228:231], v[96:99]
	v_mfma_f32_16x16x32_bf16 v[48:51], v[178:181], v[238:241], v[48:51]
	v_mfma_f32_16x16x32_bf16 v[64:67], v[186:189], v[238:241], v[64:67]
	s_setprio 0
	s_barrier
	s_add_i32 s82, s72, s97
	v_lshl_add_u64 v[190:191], s[52:53], 0, v[144:145]
	s_mov_b32 m0, s82
	ds_read_b128 v[208:211], v204 offset:16384
	ds_read_b128 v[212:215], v204 offset:17408
	ds_read_b128 v[216:219], v204 offset:18432
	ds_read_b128 v[220:223], v204 offset:19456
	ds_read_b128 v[224:227], v204 offset:20480
	ds_read_b128 v[228:231], v204 offset:21504
	ds_read_b128 v[232:235], v204 offset:22528
	ds_read_b128 v[238:241], v204 offset:23552
	global_load_lds_dwordx4 v[190:191], off
	s_add_i32 m0, s82, 0x2000
	s_add_u32 s82, s52, 0x80000
	v_lshl_add_u64 v[236:237], s[52:53], 0, v[146:147]
	s_addc_u32 s83, s53, 0
	s_add_i32 s84, s73, s97
	global_load_lds_dwordx4 v[236:237], off
	v_lshl_add_u64 v[242:243], s[82:83], 0, v[144:145]
	s_mov_b32 m0, s84
	v_lshl_add_u64 v[244:245], s[54:55], 0, v[152:153]
	global_load_lds_dwordx4 v[242:243], off
	v_lshl_add_u64 v[242:243], s[82:83], 0, v[146:147]
	s_add_i32 m0, s84, 0x2000
	s_nop 0
	global_load_lds_dwordx4 v[242:243], off
	v_lshl_add_u64 v[242:243], s[54:55], 0, v[148:149]
	s_mov_b32 m0, s25
	s_nop 0
	global_load_lds_dwordx4 v[242:243], off
	s_mov_b32 m0, s58
	s_nop 0
	global_load_lds_dwordx4 v[244:245], off
	s_waitcnt vmcnt(8)
	s_waitcnt lgkmcnt(0)
	s_barrier
; #define PG8_STAGE(bufoff, gbase, o0, o1) do { \
;         __builtin_amdgcn_global_load_lds((const unsigned*)((const char*)(gbase) + (o0)), (LAS unsigned*)(lds + (bufoff) + ldsw), 16, 0, 0); \
;         __builtin_amdgcn_global_load_lds((const unsigned*)((const char*)(gbase) + (o1)), (LAS unsigned*)(lds + (bufoff) + ldsw + 8192), 16, 0, 0); } while (0)
; #define PG8_LDA(dst, b, h) do { _Pragma("unroll") for (int m = 0; m < 4; ++m) _Pragma("unroll") for (int k = 0; k < 2; ++k) dst[m][k] = *(const LAS bf16x8*)(lds + PG8_SA(b, h) + aoff + m * 2048 + k * 1024); } while (0)
; #define PG8_LDB(dst, b, h) do { _Pragma("unroll") for (int n = 0; n < 2; ++n) _Pragma("unroll") for (int k = 0; k < 2; ++k) dst[n][k] = *(const LAS bf16x8*)(lds + PG8_SB(b, h) + boff + n * 2048 + k * 1024); } while (0)
; #define PG8_WAIT_V(n) asm volatile("s_waitcnt vmcnt(" #n ")" ::: "memory")
; #define PG8_WAIT_L(n) asm volatile("s_waitcnt lgkmcnt(" #n ")" ::: "memory")
; #define PG8_BAR __builtin_amdgcn_s_barrier()
; #define PG8_SCHED __builtin_amdgcn_sched_barrier(0)
; template <class Epi, class Sched, class Prob>
; __device__ __forceinline__ void gemm_phase(LAS unsigned char* lds, LAS unsigned char* lds_epi, const Prob g, const Sched& S, const Epi& E, int wid) {
;     ...
;             PG8_LDB(B0, 0, 0); PG8_LDB(B1, 0, 1); PG8_SCHED; PG8_LDA(At, 0, 0); PG8_STAGE(PG8_SA(1, 1), a1, cA10, cA11);
;             PG8_WAIT_V(8); PG8_WAIT_L(0); PG8_BAR; PG8_MMA(0, 0, At, B0); PG8_MMA(0, 1, At, B1); PG8_BAR; PG8_SCHED;
;             PG8_LDA(At, 0, 1); PG8_STAGE(PG8_SB(0, 0), b2, vB0, vB1); PG8_STAGE(PG8_SB(0, 1), b2 + hstepB, vB0, vB1); PG8_STAGE(PG8_SA(0, 0), a2, cA00, cA01);
;             PG8_WAIT_V(8); PG8_WAIT_L(0); PG8_BAR; PG8_MMA(1, 0, At, B0); PG8_MMA(1, 1, At, B1); PG8_BAR; PG8_SCHED;
;             PG8_LDB(B0, 1, 0); PG8_LDB(B1, 1, 1); PG8_SCHED; PG8_LDA(At, 1, 0); PG8_STAGE(PG8_SA(0, 1), a2, cA10, cA11);
;             PG8_WAIT_V(8); PG8_WAIT_L(0); PG8_BAR; PG8_MMA(0, 0, At, B0); PG8_MMA(0, 1, At, B1); PG8_BAR; PG8_SCHED;
;             PG8_LDA(At, 1, 1); PG8_STAGE(PG8_SB(1, 0), b3, vB0, vB1); PG8_STAGE(PG8_SB(1, 1), b3 + hstepB, vB0, vB1); PG8_STAGE(PG8_SA(1, 0), a3, cA00, cA01);
;             PG8_WAIT_V(8); PG8_WAIT_L(0); PG8_BAR; PG8_MMA(1, 0, At, B0); PG8_MMA(1, 1, At, B1); PG8_BAR; PG8_SCHED;
	s_setprio 1
	s_waitcnt lgkmcnt(0)
	v_mfma_f32_16x16x32_bf16 v[56:59], v[128:131], v[208:211], 0
	v_mfma_f32_16x16x32_bf16 v[72:75], v[136:139], v[208:211], 0
	v_mfma_f32_16x16x32_bf16 v[32:35], v[128:131], v[216:219], 0
	v_mfma_f32_16x16x32_bf16 v[40:43], v[136:139], v[216:219], 0
	v_mfma_f32_16x16x32_bf16 v[12:15], v[128:131], v[224:227], 0
	v_mfma_f32_16x16x32_bf16 v[20:23], v[136:139], v[224:227], 0
	v_mfma_f32_16x16x32_bf16 v[0:3], v[128:131], v[232:235], 0
	v_mfma_f32_16x16x32_bf16 v[4:7], v[136:139], v[232:235], 0
	v_mfma_f32_16x16x32_bf16 v[56:59], v[132:135], v[212:215], v[56:59]
	v_mfma_f32_16x16x32_bf16 v[72:75], v[140:143], v[212:215], v[72:75]
	v_mfma_f32_16x16x32_bf16 v[32:35], v[132:135], v[220:223], v[32:35]
	v_mfma_f32_16x16x32_bf16 v[40:43], v[140:143], v[220:223], v[40:43]
	v_mfma_f32_16x16x32_bf16 v[12:15], v[132:135], v[228:231], v[12:15]
	v_mfma_f32_16x16x32_bf16 v[20:23], v[140:143], v[228:231], v[20:23]
	v_mfma_f32_16x16x32_bf16 v[0:3], v[132:135], v[238:241], v[0:3]
	v_mfma_f32_16x16x32_bf16 v[4:7], v[140:143], v[238:241], v[4:7]
	s_setprio 0
	s_setprio 1
	v_mfma_f32_16x16x32_bf16 v[108:111], v[174:177], v[208:211], 0
	v_mfma_f32_16x16x32_bf16 v[116:119], v[182:185], v[208:211], 0
	v_mfma_f32_16x16x32_bf16 v[88:91], v[174:177], v[216:219], 0
	v_mfma_f32_16x16x32_bf16 v[100:103], v[182:185], v[216:219], 0
	v_mfma_f32_16x16x32_bf16 v[60:63], v[174:177], v[224:227], 0
	v_mfma_f32_16x16x32_bf16 v[76:79], v[182:185], v[224:227], 0
	v_mfma_f32_16x16x32_bf16 v[24:27], v[174:177], v[232:235], 0
	v_mfma_f32_16x16x32_bf16 v[44:47], v[182:185], v[232:235], 0
	v_mfma_f32_16x16x32_bf16 v[108:111], v[178:181], v[212:215], v[108:111]
	v_mfma_f32_16x16x32_bf16 v[116:119], v[186:189], v[212:215], v[116:119]
	v_mfma_f32_16x16x32_bf16 v[88:91], v[178:181], v[220:223], v[88:91]
	v_mfma_f32_16x16x32_bf16 v[100:103], v[186:189], v[220:223], v[100:103]
	v_mfma_f32_16x16x32_bf16 v[60:63], v[178:181], v[228:231], v[60:63]
	v_mfma_f32_16x16x32_bf16 v[76:79], v[186:189], v[228:231], v[76:79]
	v_mfma_f32_16x16x32_bf16 v[24:27], v[178:181], v[238:241], v[24:27]
	v_mfma_f32_16x16x32_bf16 v[44:47], v[186:189], v[238:241], v[44:47]
	s_setprio 0
	s_barrier
	s_add_i32 s82, 0, 0x18000
	s_add_i32 s83, 0, 0x1c000
	v_add_u32_e32 v140, s82, v194
	v_add_u32_e32 v156, s83, v194
	ds_read_b128 v[128:131], v140
	ds_read_b128 v[132:135], v140 offset:1024
	ds_read_b128 v[136:139], v140 offset:2048
	ds_read_b128 v[140:143], v140 offset:3072
	ds_read_b128 v[174:177], v156
	ds_read_b128 v[178:181], v156 offset:1024
	ds_read_b128 v[182:185], v156 offset:2048
	ds_read_b128 v[186:189], v156 offset:3072
	s_mov_b32 m0, s59
	v_lshl_add_u64 v[246:247], s[54:55], 0, v[150:151]
	ds_read_b128 v[208:211], v204 offset:32768
	ds_read_b128 v[212:215], v204 offset:33792
	ds_read_b128 v[216:219], v204 offset:34816
	ds_read_b128 v[220:223], v204 offset:35840
	ds_read_b128 v[224:227], v204 offset:36864
	ds_read_b128 v[228:231], v204 offset:37888
	ds_read_b128 v[232:235], v204 offset:38912
	ds_read_b128 v[238:241], v204 offset:39936
	global_load_lds_dwordx4 v[246:247], off
	v_lshl_add_u64 v[246:247], s[54:55], 0, v[154:155]
	s_mov_b32 m0, s60
	s_nop 0
	global_load_lds_dwordx4 v[246:247], off
	s_waitcnt vmcnt(8)
	s_waitcnt lgkmcnt(0)
	s_barrier
	s_setprio 1
	s_waitcnt lgkmcnt(0)
	v_mfma_f32_16x16x32_bf16 v[80:83], v[128:131], v[208:211], v[80:83]
	v_mfma_f32_16x16x32_bf16 v[92:95], v[136:139], v[208:211], v[92:95]
	v_mfma_f32_16x16x32_bf16 v[52:55], v[128:131], v[216:219], v[52:55]
	v_mfma_f32_16x16x32_bf16 v[68:71], v[136:139], v[216:219], v[68:71]
	v_mfma_f32_16x16x32_bf16 v[28:31], v[128:131], v[224:227], v[28:31]
	v_mfma_f32_16x16x32_bf16 v[36:39], v[136:139], v[224:227], v[36:39]
	v_mfma_f32_16x16x32_bf16 v[8:11], v[128:131], v[232:235], v[8:11]
	v_mfma_f32_16x16x32_bf16 v[16:19], v[136:139], v[232:235], v[16:19]
	v_mfma_f32_16x16x32_bf16 v[80:83], v[132:135], v[212:215], v[80:83]
	v_mfma_f32_16x16x32_bf16 v[92:95], v[140:143], v[212:215], v[92:95]
	v_mfma_f32_16x16x32_bf16 v[52:55], v[132:135], v[220:223], v[52:55]
	v_mfma_f32_16x16x32_bf16 v[68:71], v[140:143], v[220:223], v[68:71]
	v_mfma_f32_16x16x32_bf16 v[28:31], v[132:135], v[228:231], v[28:31]
	v_mfma_f32_16x16x32_bf16 v[36:39], v[140:143], v[228:231], v[36:39]
	v_mfma_f32_16x16x32_bf16 v[8:11], v[132:135], v[238:241], v[8:11]
	v_mfma_f32_16x16x32_bf16 v[16:19], v[140:143], v[238:241], v[16:19]
	s_setprio 0
	s_setprio 1
	v_mfma_f32_16x16x32_bf16 v[120:123], v[174:177], v[208:211], v[120:123]
	v_mfma_f32_16x16x32_bf16 v[124:127], v[182:185], v[208:211], v[124:127]
	v_mfma_f32_16x16x32_bf16 v[104:107], v[174:177], v[216:219], v[104:107]
	v_mfma_f32_16x16x32_bf16 v[112:115], v[182:185], v[216:219], v[112:115]
	v_mfma_f32_16x16x32_bf16 v[84:87], v[174:177], v[224:227], v[84:87]
	v_mfma_f32_16x16x32_bf16 v[96:99], v[182:185], v[224:227], v[96:99]
	v_mfma_f32_16x16x32_bf16 v[48:51], v[174:177], v[232:235], v[48:51]
	v_mfma_f32_16x16x32_bf16 v[64:67], v[182:185], v[232:235], v[64:67]
	v_mfma_f32_16x16x32_bf16 v[120:123], v[178:181], v[212:215], v[120:123]
	v_mfma_f32_16x16x32_bf16 v[124:127], v[186:189], v[212:215], v[124:127]
	v_mfma_f32_16x16x32_bf16 v[104:107], v[178:181], v[220:223], v[104:107]
	v_mfma_f32_16x16x32_bf16 v[112:115], v[186:189], v[220:223], v[112:115]
	v_mfma_f32_16x16x32_bf16 v[84:87], v[178:181], v[228:231], v[84:87]
	v_mfma_f32_16x16x32_bf16 v[96:99], v[186:189], v[228:231], v[96:99]
	v_mfma_f32_16x16x32_bf16 v[48:51], v[178:181], v[238:241], v[48:51]
	v_mfma_f32_16x16x32_bf16 v[64:67], v[186:189], v[238:241], v[64:67]
	s_setprio 0
	s_barrier
; #define PG8_STAGE(bufoff, gbase, o0, o1) do { \
;         __builtin_amdgcn_global_load_lds((const unsigned*)((const char*)(gbase) + (o0)), (LAS unsigned*)(lds + (bufoff) + ldsw), 16, 0, 0); \
;         __builtin_amdgcn_global_load_lds((const unsigned*)((const char*)(gbase) + (o1)), (LAS unsigned*)(lds + (bufoff) + ldsw + 8192), 16, 0, 0); } while (0)
; #define PG8_LDA(dst, b, h) do { _Pragma("unroll") for (int m = 0; m < 4; ++m) _Pragma("unroll") for (int k = 0; k < 2; ++k) dst[m][k] = *(const LAS bf16x8*)(lds + PG8_SA(b, h) + aoff + m * 2048 + k * 1024); } while (0)
; #define PG8_WAIT_V(n) asm volatile("s_waitcnt vmcnt(" #n ")" ::: "memory")
; #define PG8_WAIT_L(n) asm volatile("s_waitcnt lgkmcnt(" #n ")" ::: "memory")
; #define PG8_BAR __builtin_amdgcn_s_barrier()
; #define PG8_SCHED __builtin_amdgcn_sched_barrier(0)
; template <class Epi, class Sched, class Prob>
; __device__ __forceinline__ void gemm_phase(LAS unsigned char* lds, LAS unsigned char* lds_epi, const Prob g, const Sched& S, const Epi& E, int wid) {
;     ...
;             PG8_LDA(At, 1, 1); PG8_STAGE(PG8_SB(1, 0), b3, vB0, vB1); PG8_STAGE(PG8_SB(1, 1), b3 + hstepB, vB0, vB1); PG8_STAGE(PG8_SA(1, 0), a3, cA00, cA01);
;             PG8_WAIT_V(8); PG8_WAIT_L(0); PG8_BAR; PG8_MMA(1, 0, At, B0); PG8_MMA(1, 1, At, B1); PG8_BAR; PG8_SCHED;
	s_add_i32 s54, s82, s97
	v_lshl_add_u64 v[190:191], v[190:191], 0, s[20:21]
	s_mov_b32 m0, s54
	ds_read_b128 v[208:211], v204 offset:49152
	ds_read_b128 v[212:215], v204 offset:50176
	ds_read_b128 v[216:219], v204 offset:51200
	ds_read_b128 v[220:223], v204 offset:52224
	ds_read_b128 v[224:227], v204 offset:53248
	ds_read_b128 v[228:231], v204 offset:54272
	ds_read_b128 v[232:235], v204 offset:55296
	ds_read_b128 v[238:241], v204 offset:56320
	global_load_lds_dwordx4 v[190:191], off
	s_add_i32 m0, s54, 0x2000
	s_add_u32 s52, s52, 0x80080
	v_lshl_add_u64 v[190:191], v[236:237], 0, s[20:21]
	s_addc_u32 s53, s53, 0
	s_add_i32 s54, s83, s97
	global_load_lds_dwordx4 v[190:191], off
	v_lshl_add_u64 v[190:191], s[52:53], 0, v[144:145]
	s_mov_b32 m0, s54
	s_nop 0
	global_load_lds_dwordx4 v[190:191], off
	v_lshl_add_u64 v[190:191], s[52:53], 0, v[146:147]
	s_add_i32 m0, s54, 0x2000
	s_nop 0
	global_load_lds_dwordx4 v[190:191], off
	v_lshl_add_u64 v[190:191], v[242:243], 0, s[20:21]
	s_mov_b32 m0, s70
	s_nop 0
	global_load_lds_dwordx4 v[190:191], off
	v_lshl_add_u64 v[190:191], v[244:245], 0, s[20:21]
	s_mov_b32 m0, s71
	s_nop 0
	global_load_lds_dwordx4 v[190:191], off
	s_waitcnt vmcnt(8)
	s_waitcnt lgkmcnt(0)
	s_barrier
	s_setprio 1
	s_waitcnt lgkmcnt(0)
	v_mfma_f32_16x16x32_bf16 v[56:59], v[128:131], v[208:211], v[56:59]
	v_mfma_f32_16x16x32_bf16 v[72:75], v[136:139], v[208:211], v[72:75]
	v_mfma_f32_16x16x32_bf16 v[32:35], v[128:131], v[216:219], v[32:35]
	v_mfma_f32_16x16x32_bf16 v[40:43], v[136:139], v[216:219], v[40:43]
	v_mfma_f32_16x16x32_bf16 v[12:15], v[128:131], v[224:227], v[12:15]
	v_mfma_f32_16x16x32_bf16 v[20:23], v[136:139], v[224:227], v[20:23]
	v_mfma_f32_16x16x32_bf16 v[0:3], v[128:131], v[232:235], v[0:3]
	v_mfma_f32_16x16x32_bf16 v[4:7], v[136:139], v[232:235], v[4:7]
	v_mfma_f32_16x16x32_bf16 v[56:59], v[132:135], v[212:215], v[56:59]
	v_mfma_f32_16x16x32_bf16 v[72:75], v[140:143], v[212:215], v[72:75]
	v_mfma_f32_16x16x32_bf16 v[32:35], v[132:135], v[220:223], v[32:35]
	v_mfma_f32_16x16x32_bf16 v[40:43], v[140:143], v[220:223], v[40:43]
	v_mfma_f32_16x16x32_bf16 v[12:15], v[132:135], v[228:231], v[12:15]
	v_mfma_f32_16x16x32_bf16 v[20:23], v[140:143], v[228:231], v[20:23]
	v_mfma_f32_16x16x32_bf16 v[0:3], v[132:135], v[238:241], v[0:3]
	v_mfma_f32_16x16x32_bf16 v[4:7], v[140:143], v[238:241], v[4:7]
	s_setprio 0
	s_setprio 1
	v_mfma_f32_16x16x32_bf16 v[108:111], v[174:177], v[208:211], v[108:111]
	v_mfma_f32_16x16x32_bf16 v[116:119], v[182:185], v[208:211], v[116:119]
	v_mfma_f32_16x16x32_bf16 v[88:91], v[174:177], v[216:219], v[88:91]
	v_mfma_f32_16x16x32_bf16 v[100:103], v[182:185], v[216:219], v[100:103]
	v_mfma_f32_16x16x32_bf16 v[60:63], v[174:177], v[224:227], v[60:63]
	v_mfma_f32_16x16x32_bf16 v[76:79], v[182:185], v[224:227], v[76:79]
	v_mfma_f32_16x16x32_bf16 v[24:27], v[174:177], v[232:235], v[24:27]
	v_mfma_f32_16x16x32_bf16 v[44:47], v[182:185], v[232:235], v[44:47]
	v_mfma_f32_16x16x32_bf16 v[108:111], v[178:181], v[212:215], v[108:111]
	v_mfma_f32_16x16x32_bf16 v[116:119], v[186:189], v[212:215], v[116:119]
	v_mfma_f32_16x16x32_bf16 v[88:91], v[178:181], v[220:223], v[88:91]
	v_mfma_f32_16x16x32_bf16 v[100:103], v[186:189], v[220:223], v[100:103]
	v_mfma_f32_16x16x32_bf16 v[60:63], v[178:181], v[228:231], v[60:63]
	v_mfma_f32_16x16x32_bf16 v[76:79], v[186:189], v[228:231], v[76:79]
	v_mfma_f32_16x16x32_bf16 v[24:27], v[178:181], v[238:241], v[24:27]
	v_mfma_f32_16x16x32_bf16 v[44:47], v[186:189], v[238:241], v[44:47]
	s_setprio 0
	s_barrier
	s_add_i32 s81, s81, 2
	s_add_u32 s14, s14, 0x100
	s_addc_u32 s15, s15, 0
	s_add_u32 s79, s79, 0x100
	s_addc_u32 s80, s80, 0
	s_cmp_gt_u32 s81, 29

; #define PG8_STAGE(bufoff, gbase, o0, o1) do { \
;         __builtin_amdgcn_global_load_lds((const unsigned*)((const char*)(gbase) + (o0)), (LAS unsigned*)(lds + (bufoff) + ldsw), 16, 0, 0); \
;         __builtin_amdgcn_global_load_lds((const unsigned*)((const char*)(gbase) + (o1)), (LAS unsigned*)(lds + (bufoff) + ldsw + 8192), 16, 0, 0); } while (0)
; #define PG8_LDA(dst, b, h) do { _Pragma("unroll") for (int m = 0; m < 4; ++m) _Pragma("unroll") for (int k = 0; k < 2; ++k) dst[m][k] = *(const LAS bf16x8*)(lds + PG8_SA(b, h) + aoff + m * 2048 + k * 1024); } while (0)
; #define PG8_LDB(dst, b, h) do { _Pragma("unroll") for (int n = 0; n < 2; ++n) _Pragma("unroll") for (int k = 0; k < 2; ++k) dst[n][k] = *(const LAS bf16x8*)(lds + PG8_SB(b, h) + boff + n * 2048 + k * 1024); } while (0)
; #define PG8_WAIT_V(n) asm volatile("s_waitcnt vmcnt(" #n ")" ::: "memory")
; #define PG8_WAIT_L(n) asm volatile("s_waitcnt lgkmcnt(" #n ")" ::: "memory")
; #define PG8_BAR __builtin_amdgcn_s_barrier()
; #define PG8_SCHED __builtin_amdgcn_sched_barrier(0)
; template <class Epi, class Sched, class Prob>
; __device__ __forceinline__ void gemm_phase(LAS unsigned char* lds, LAS unsigned char* lds_epi, const Prob g, const Sched& S, const Epi& E, int wid) {
;     ...
;         const bool has_next = S.next(ui + 1, nxt);
;         const char* nA = has_next ? g.a_base(nxt) : cA; const char* nB = has_next ? g.b_base(nxt) : cB;
; _Pragma("clang loop unroll(disable)")
;         for (int t = 0; t < nt; t += 2) {
;             const bool last = (t == nt - 2);
;             const char* a1 = cA + (size_t)(t + 1) * kstep;
;             const char* a2 = last ? nA : cA + (size_t)(t + 2) * kstep; const char* b2 = last ? nB : cB + (size_t)(t + 2) * kstep;
;             const char* a3 = a2 + kstep; const char* b3 = b2 + kstep;
;             PG8_LDB(B0, 0, 0); PG8_LDB(B1, 0, 1); PG8_SCHED; PG8_LDA(At, 0, 0); PG8_STAGE(PG8_SA(1, 1), a1, cA10, cA11);
;             PG8_WAIT_V(8); PG8_WAIT_L(0); PG8_BAR; PG8_MMA(0, 0, At, B0); PG8_MMA(0, 1, At, B1); PG8_BAR; PG8_SCHED;
;             PG8_LDA(At, 0, 1); PG8_STAGE(PG8_SB(0, 0), b2, vB0, vB1); PG8_STAGE(PG8_SB(0, 1), b2 + hstepB, vB0, vB1); PG8_STAGE(PG8_SA(0, 0), a2, cA00, cA01);
;             PG8_WAIT_V(8); PG8_WAIT_L(0); PG8_BAR; PG8_MMA(1, 0, At, B0); PG8_MMA(1, 1, At, B1); PG8_BAR; PG8_SCHED;
.LBB0_1247:
	s_ashr_i32 s3, s2, 31
	s_lshl_b64 s[24:25], s[2:3], 19
	s_add_u32 s24, s36, s24
	s_addc_u32 s25, s37, s25
	s_and_b64 s[26:27], s[22:23], exec
	s_cselect_b32 s3, s25, s11
	s_cselect_b32 s54, s24, s10
	s_ashr_i32 s21, s20, 31
	s_lshl_b64 s[26:27], s[20:21], 19
	s_add_u32 s26, s40, s26
	s_addc_u32 s27, s41, s27
	s_and_b64 s[34:35], s[22:23], exec
	s_cselect_b32 s21, s27, s31
	s_cselect_b32 s55, s26, s30
	s_add_u32 s10, s10, 0x80
	s_addc_u32 s11, s11, 0
	s_add_u32 s56, s30, 0x100
	v_mov_b32_e32 v32, 0
	s_addc_u32 s58, s31, 0
	s_mov_b32 s59, -2
	ds_read_b128 v[24:27], v194
	ds_read_b128 v[28:31], v194 offset:1024
	ds_read_b128 v[16:19], v194 offset:2048
	ds_read_b128 v[20:23], v194 offset:3072
	ds_read_b128 v[8:11], v195
	ds_read_b128 v[12:15], v195 offset:1024
	ds_read_b128 v[0:3], v195 offset:2048
	ds_read_b128 v[4:7], v195 offset:3072
	s_add_u32 s30, s10, 0x80
	s_addc_u32 s31, s11, 0
	s_cmp_eq_u32 s59, 12
	s_cselect_b32 s35, s3, s31
	s_cselect_b32 s34, s54, s30
	s_cselect_b32 s31, s21, s58
	s_cselect_b32 s30, s55, s56
	v_lshl_add_u64 v[224:225], s[10:11], 0, v[178:179]
	s_add_i32 m0, s29, 0xc000
	ds_read_b128 v[182:185], v196
	ds_read_b128 v[186:189], v196 offset:1024
	ds_read_b128 v[200:203], v196 offset:2048
	ds_read_b128 v[204:207], v196 offset:3072
	ds_read_b128 v[208:211], v196 offset:4096
	ds_read_b128 v[212:215], v196 offset:5120
	ds_read_b128 v[216:219], v196 offset:6144
	ds_read_b128 v[220:223], v196 offset:7168
	global_load_lds_dwordx4 v[224:225], off
	v_lshl_add_u64 v[224:225], s[10:11], 0, v[176:177]
	s_add_i32 m0, s29, 0xe000
	s_nop 0
	global_load_lds_dwordx4 v[224:225], off
	s_waitcnt vmcnt(8)
	s_waitcnt lgkmcnt(0)
	s_barrier
	s_setprio 1
	s_waitcnt lgkmcnt(0)
	v_mfma_f32_16x16x128_f8f6f4 v[156:159], v[24:31], v[182:189], 0
	v_mfma_f32_16x16x128_f8f6f4 v[144:147], v[16:23], v[182:189], 0
	v_mfma_f32_16x16x128_f8f6f4 v[140:143], v[24:31], v[200:207], 0
	v_mfma_f32_16x16x128_f8f6f4 v[132:135], v[16:23], v[200:207], 0
	v_mfma_f32_16x16x128_f8f6f4 v[124:127], v[24:31], v[208:215], 0
	v_mfma_f32_16x16x128_f8f6f4 v[116:119], v[16:23], v[208:215], 0
	v_mfma_f32_16x16x128_f8f6f4 v[108:111], v[24:31], v[216:223], 0
	v_mfma_f32_16x16x128_f8f6f4 v[100:103], v[16:23], v[216:223], 0
	s_setprio 0
	s_setprio 1
	v_mfma_f32_16x16x128_f8f6f4 v[152:155], v[8:15], v[182:189], 0
	v_mfma_f32_16x16x128_f8f6f4 v[148:151], v[0:7], v[182:189], 0
	v_mfma_f32_16x16x128_f8f6f4 v[136:139], v[8:15], v[200:207], 0
	v_mfma_f32_16x16x128_f8f6f4 v[128:131], v[0:7], v[200:207], 0
	v_mfma_f32_16x16x128_f8f6f4 v[120:123], v[8:15], v[208:215], 0
	v_mfma_f32_16x16x128_f8f6f4 v[112:115], v[0:7], v[208:215], 0
	v_mfma_f32_16x16x128_f8f6f4 v[104:107], v[8:15], v[216:223], 0
	v_mfma_f32_16x16x128_f8f6f4 v[96:99], v[0:7], v[216:223], 0
	s_setprio 0
	s_barrier
	s_add_i32 s60, s50, s97
	v_lshl_add_u64 v[182:183], s[30:31], 0, v[162:163]
	s_mov_b32 m0, s60
	ds_read_b128 v[200:203], v196 offset:16384
	ds_read_b128 v[204:207], v196 offset:17408
	ds_read_b128 v[208:211], v196 offset:18432
	ds_read_b128 v[212:215], v196 offset:19456
	ds_read_b128 v[216:219], v196 offset:20480
	ds_read_b128 v[220:223], v196 offset:21504
	ds_read_b128 v[224:227], v196 offset:22528
	ds_read_b128 v[228:231], v196 offset:23552
	global_load_lds_dwordx4 v[182:183], off
	s_add_i32 m0, s60, 0x2000
	s_add_u32 s60, s30, 0x40000
	v_lshl_add_u64 v[184:185], s[30:31], 0, v[160:161]
	s_addc_u32 s61, s31, 0
	s_add_i32 s62, s51, s97
	global_load_lds_dwordx4 v[184:185], off
	v_lshl_add_u64 v[186:187], s[60:61], 0, v[162:163]
	s_mov_b32 m0, s62
	v_lshl_add_u64 v[188:189], s[34:35], 0, v[168:169]
	global_load_lds_dwordx4 v[186:187], off
	v_lshl_add_u64 v[186:187], s[60:61], 0, v[160:161]
	s_add_i32 m0, s62, 0x2000
	s_nop 0
	global_load_lds_dwordx4 v[186:187], off
	v_lshl_add_u64 v[186:187], s[34:35], 0, v[164:165]
	s_mov_b32 m0, s29
	s_nop 0
	global_load_lds_dwordx4 v[186:187], off
	s_mov_b32 m0, s43
	s_nop 0
	global_load_lds_dwordx4 v[188:189], off
	s_waitcnt vmcnt(8)
	s_waitcnt lgkmcnt(0)
	s_barrier
	s_setprio 1
	s_waitcnt lgkmcnt(0)
	v_mfma_f32_16x16x128_f8f6f4 v[92:95], v[24:31], v[200:207], 0
	v_mfma_f32_16x16x128_f8f6f4 v[84:87], v[16:23], v[200:207], 0
	v_mfma_f32_16x16x128_f8f6f4 v[76:79], v[24:31], v[208:215], 0
	v_mfma_f32_16x16x128_f8f6f4 v[68:71], v[16:23], v[208:215], 0
	v_mfma_f32_16x16x128_f8f6f4 v[60:63], v[24:31], v[216:223], 0
	v_mfma_f32_16x16x128_f8f6f4 v[52:55], v[16:23], v[216:223], 0
	v_mfma_f32_16x16x128_f8f6f4 v[44:47], v[24:31], v[224:231], 0
	v_mfma_f32_16x16x128_f8f6f4 v[36:39], v[16:23], v[224:231], 0
	s_setprio 0
	s_setprio 1
	v_mfma_f32_16x16x128_f8f6f4 v[88:91], v[8:15], v[200:207], 0
	v_mfma_f32_16x16x128_f8f6f4 v[80:83], v[0:7], v[200:207], 0
	v_mfma_f32_16x16x128_f8f6f4 v[72:75], v[8:15], v[208:215], 0
	v_mfma_f32_16x16x128_f8f6f4 v[64:67], v[0:7], v[208:215], 0
	v_mfma_f32_16x16x128_f8f6f4 v[56:59], v[8:15], v[216:223], 0
	v_mfma_f32_16x16x128_f8f6f4 v[48:51], v[0:7], v[216:223], 0
	v_mfma_f32_16x16x128_f8f6f4 v[40:43], v[8:15], v[224:231], 0
	v_mfma_f32_16x16x128_f8f6f4 v[32:35], v[0:7], v[224:231], 0
	s_setprio 0
	s_barrier
; #define PG8_STAGE(bufoff, gbase, o0, o1) do { \
;         __builtin_amdgcn_global_load_lds((const unsigned*)((const char*)(gbase) + (o0)), (LAS unsigned*)(lds + (bufoff) + ldsw), 16, 0, 0); \
;         __builtin_amdgcn_global_load_lds((const unsigned*)((const char*)(gbase) + (o1)), (LAS unsigned*)(lds + (bufoff) + ldsw + 8192), 16, 0, 0); } while (0)
; #define PG8_LDA(dst, b, h) do { _Pragma("unroll") for (int m = 0; m < 4; ++m) _Pragma("unroll") for (int k = 0; k < 2; ++k) dst[m][k] = *(const LAS bf16x8*)(lds + PG8_SA(b, h) + aoff + m * 2048 + k * 1024); } while (0)
; #define PG8_LDB(dst, b, h) do { _Pragma("unroll") for (int n = 0; n < 2; ++n) _Pragma("unroll") for (int k = 0; k < 2; ++k) dst[n][k] = *(const LAS bf16x8*)(lds + PG8_SB(b, h) + boff + n * 2048 + k * 1024); } while (0)
; #define PG8_WAIT_V(n) asm volatile("s_waitcnt vmcnt(" #n ")" ::: "memory")
; #define PG8_WAIT_L(n) asm volatile("s_waitcnt lgkmcnt(" #n ")" ::: "memory")
; #define PG8_BAR __builtin_amdgcn_s_barrier()
; #define PG8_SCHED __builtin_amdgcn_sched_barrier(0)
; template <class Epi, class Sched, class Prob>
; __device__ __forceinline__ void gemm_phase(LAS unsigned char* lds, LAS unsigned char* lds_epi, const Prob g, const Sched& S, const Epi& E, int wid) {
;     ...
;             PG8_LDB(B0, 1, 0); PG8_LDB(B1, 1, 1); PG8_SCHED; PG8_LDA(At, 1, 0); PG8_STAGE(PG8_SA(0, 1), a2, cA10, cA11);
;             PG8_WAIT_V(8); PG8_WAIT_L(0); PG8_BAR; PG8_MMA(0, 0, At, B0); PG8_MMA(0, 1, At, B1); PG8_BAR; PG8_SCHED;
;             PG8_LDA(At, 1, 1); PG8_STAGE(PG8_SB(1, 0), b3, vB0, vB1); PG8_STAGE(PG8_SB(1, 1), b3 + hstepB, vB0, vB1); PG8_STAGE(PG8_SA(1, 0), a3, cA00, cA01);
;             PG8_WAIT_V(8); PG8_WAIT_L(0); PG8_BAR; PG8_MMA(1, 0, At, B0); PG8_MMA(1, 1, At, B1); PG8_BAR; PG8_SCHED;
	s_add_i32 s60, 0, 0x18000
	s_add_i32 s61, 0, 0x1c000
	v_add_u32_e32 v12, s60, v191
	v_add_u32_e32 v28, s61, v191
	ds_read_b128 v[0:3], v12
	ds_read_b128 v[4:7], v12 offset:1024
	ds_read_b128 v[8:11], v12 offset:2048
	ds_read_b128 v[12:15], v12 offset:3072
	ds_read_b128 v[16:19], v28
	ds_read_b128 v[20:23], v28 offset:1024
	ds_read_b128 v[24:27], v28 offset:2048
	ds_read_b128 v[28:31], v28 offset:3072
	s_mov_b32 m0, s44
	v_lshl_add_u64 v[232:233], s[34:35], 0, v[166:167]
	ds_read_b128 v[200:203], v196 offset:32768
	ds_read_b128 v[204:207], v196 offset:33792
	ds_read_b128 v[208:211], v196 offset:34816
	ds_read_b128 v[212:215], v196 offset:35840
	ds_read_b128 v[216:219], v196 offset:36864
	ds_read_b128 v[220:223], v196 offset:37888
	ds_read_b128 v[224:227], v196 offset:38912
	ds_read_b128 v[228:231], v196 offset:39936
	global_load_lds_dwordx4 v[232:233], off
	v_lshl_add_u64 v[232:233], s[34:35], 0, v[170:171]
	s_mov_b32 m0, s45
	s_nop 0
	global_load_lds_dwordx4 v[232:233], off
	s_waitcnt vmcnt(8)
	s_waitcnt lgkmcnt(0)
	s_barrier
	s_setprio 1
	s_waitcnt lgkmcnt(0)
	v_mfma_f32_16x16x128_f8f6f4 v[156:159], v[0:7], v[200:207], v[156:159]
	v_mfma_f32_16x16x128_f8f6f4 v[144:147], v[8:15], v[200:207], v[144:147]
	v_mfma_f32_16x16x128_f8f6f4 v[140:143], v[0:7], v[208:215], v[140:143]
	v_mfma_f32_16x16x128_f8f6f4 v[132:135], v[8:15], v[208:215], v[132:135]
	v_mfma_f32_16x16x128_f8f6f4 v[124:127], v[0:7], v[216:223], v[124:127]
	v_mfma_f32_16x16x128_f8f6f4 v[116:119], v[8:15], v[216:223], v[116:119]
	v_mfma_f32_16x16x128_f8f6f4 v[108:111], v[0:7], v[224:231], v[108:111]
	v_mfma_f32_16x16x128_f8f6f4 v[100:103], v[8:15], v[224:231], v[100:103]
	s_setprio 0
	s_setprio 1
	v_mfma_f32_16x16x128_f8f6f4 v[152:155], v[16:23], v[200:207], v[152:155]
	v_mfma_f32_16x16x128_f8f6f4 v[148:151], v[24:31], v[200:207], v[148:151]
	v_mfma_f32_16x16x128_f8f6f4 v[136:139], v[16:23], v[208:215], v[136:139]
	v_mfma_f32_16x16x128_f8f6f4 v[128:131], v[24:31], v[208:215], v[128:131]
	v_mfma_f32_16x16x128_f8f6f4 v[120:123], v[16:23], v[216:223], v[120:123]
	v_mfma_f32_16x16x128_f8f6f4 v[112:115], v[24:31], v[216:223], v[112:115]
	v_mfma_f32_16x16x128_f8f6f4 v[104:107], v[16:23], v[224:231], v[104:107]
	v_mfma_f32_16x16x128_f8f6f4 v[96:99], v[24:31], v[224:231], v[96:99]
	s_setprio 0
	s_barrier
	s_add_i32 s34, s60, s97
	v_lshl_add_u64 v[182:183], v[182:183], 0, s[14:15]
	s_mov_b32 m0, s34
	ds_read_b128 v[200:203], v196 offset:49152
	ds_read_b128 v[204:207], v196 offset:50176
	ds_read_b128 v[208:211], v196 offset:51200
	ds_read_b128 v[212:215], v196 offset:52224
	ds_read_b128 v[216:219], v196 offset:53248
	ds_read_b128 v[220:223], v196 offset:54272
	ds_read_b128 v[224:227], v196 offset:55296
	ds_read_b128 v[228:231], v196 offset:56320
	global_load_lds_dwordx4 v[182:183], off
	s_add_i32 m0, s34, 0x2000
	s_add_u32 s30, s30, 0x40080
	v_lshl_add_u64 v[182:183], v[184:185], 0, s[14:15]
	s_addc_u32 s31, s31, 0
	s_add_i32 s34, s61, s97
	global_load_lds_dwordx4 v[182:183], off
	v_lshl_add_u64 v[182:183], s[30:31], 0, v[162:163]
	s_mov_b32 m0, s34
	s_nop 0
	global_load_lds_dwordx4 v[182:183], off
	v_lshl_add_u64 v[182:183], s[30:31], 0, v[160:161]
	s_add_i32 m0, s34, 0x2000
	s_nop 0
	global_load_lds_dwordx4 v[182:183], off
	v_lshl_add_u64 v[182:183], v[186:187], 0, s[14:15]
	s_mov_b32 m0, s48
	s_nop 0
	global_load_lds_dwordx4 v[182:183], off
	v_lshl_add_u64 v[182:183], v[188:189], 0, s[14:15]
	s_mov_b32 m0, s49
	s_nop 0
	global_load_lds_dwordx4 v[182:183], off
	s_waitcnt vmcnt(8)
	s_waitcnt lgkmcnt(0)
	s_barrier
	s_setprio 1
	s_waitcnt lgkmcnt(0)
	v_mfma_f32_16x16x128_f8f6f4 v[92:95], v[0:7], v[200:207], v[92:95]
	v_mfma_f32_16x16x128_f8f6f4 v[84:87], v[8:15], v[200:207], v[84:87]
	v_mfma_f32_16x16x128_f8f6f4 v[76:79], v[0:7], v[208:215], v[76:79]
	v_mfma_f32_16x16x128_f8f6f4 v[68:71], v[8:15], v[208:215], v[68:71]
	v_mfma_f32_16x16x128_f8f6f4 v[60:63], v[0:7], v[216:223], v[60:63]
	v_mfma_f32_16x16x128_f8f6f4 v[52:55], v[8:15], v[216:223], v[52:55]
	v_mfma_f32_16x16x128_f8f6f4 v[44:47], v[0:7], v[224:231], v[44:47]
	v_mfma_f32_16x16x128_f8f6f4 v[36:39], v[8:15], v[224:231], v[36:39]
	s_setprio 0
	s_setprio 1
	v_mfma_f32_16x16x128_f8f6f4 v[88:91], v[16:23], v[200:207], v[88:91]
	v_mfma_f32_16x16x128_f8f6f4 v[80:83], v[24:31], v[200:207], v[80:83]
	v_mfma_f32_16x16x128_f8f6f4 v[72:75], v[16:23], v[208:215], v[72:75]
	v_mfma_f32_16x16x128_f8f6f4 v[64:67], v[24:31], v[208:215], v[64:67]
	v_mfma_f32_16x16x128_f8f6f4 v[56:59], v[16:23], v[216:223], v[56:59]
	v_mfma_f32_16x16x128_f8f6f4 v[48:51], v[24:31], v[216:223], v[48:51]
	v_mfma_f32_16x16x128_f8f6f4 v[40:43], v[16:23], v[224:231], v[40:43]
	v_mfma_f32_16x16x128_f8f6f4 v[32:35], v[24:31], v[224:231], v[32:35]
	s_setprio 0
	s_barrier
	s_add_i32 s59, s59, 2
	s_add_u32 s10, s10, 0x100
	s_addc_u32 s11, s11, 0
	s_add_u32 s56, s56, 0x100
	s_addc_u32 s58, s58, 0
	s_cmp_gt_u32 s59, 13

; #define PG8_STAGE(bufoff, gbase, o0, o1) do { \
;         __builtin_amdgcn_global_load_lds((const unsigned*)((const char*)(gbase) + (o0)), (LAS unsigned*)(lds + (bufoff) + ldsw), 16, 0, 0); \
;         __builtin_amdgcn_global_load_lds((const unsigned*)((const char*)(gbase) + (o1)), (LAS unsigned*)(lds + (bufoff) + ldsw + 8192), 16, 0, 0); } while (0)
; #define PG8_LDA(dst, b, h) do { _Pragma("unroll") for (int m = 0; m < 4; ++m) _Pragma("unroll") for (int k = 0; k < 2; ++k) dst[m][k] = *(const LAS bf16x8*)(lds + PG8_SA(b, h) + aoff + m * 2048 + k * 1024); } while (0)
; #define PG8_LDB(dst, b, h) do { _Pragma("unroll") for (int n = 0; n < 2; ++n) _Pragma("unroll") for (int k = 0; k < 2; ++k) dst[n][k] = *(const LAS bf16x8*)(lds + PG8_SB(b, h) + boff + n * 2048 + k * 1024); } while (0)
; #define PG8_WAIT_V(n) asm volatile("s_waitcnt vmcnt(" #n ")" ::: "memory")
; #define PG8_WAIT_L(n) asm volatile("s_waitcnt lgkmcnt(" #n ")" ::: "memory")
; #define PG8_BAR __builtin_amdgcn_s_barrier()
; #define PG8_SCHED __builtin_amdgcn_sched_barrier(0)
; template <class Epi, class Sched, class Prob>
; __device__ __forceinline__ void gemm_phase(LAS unsigned char* lds, LAS unsigned char* lds_epi, const Prob g, const Sched& S, const Epi& E, int wid) {
;     ...
;         const bool has_next = S.next(ui + 1, nxt);
;         const char* nA = has_next ? g.a_base(nxt) : cA; const char* nB = has_next ? g.b_base(nxt) : cB;
; _Pragma("clang loop unroll(disable)")
;         for (int t = 0; t < nt; t += 2) {
;             const bool last = (t == nt - 2);
;             const char* a1 = cA + (size_t)(t + 1) * kstep;
;             const char* a2 = last ? nA : cA + (size_t)(t + 2) * kstep; const char* b2 = last ? nB : cB + (size_t)(t + 2) * kstep;
;             const char* a3 = a2 + kstep; const char* b3 = b2 + kstep;
;             PG8_LDB(B0, 0, 0); PG8_LDB(B1, 0, 1); PG8_SCHED; PG8_LDA(At, 0, 0); PG8_STAGE(PG8_SA(1, 1), a1, cA10, cA11);
;             PG8_WAIT_V(8); PG8_WAIT_L(0); PG8_BAR; PG8_MMA(0, 0, At, B0); PG8_MMA(0, 1, At, B1); PG8_BAR; PG8_SCHED;
;             PG8_LDA(At, 0, 1); PG8_STAGE(PG8_SB(0, 0), b2, vB0, vB1); PG8_STAGE(PG8_SB(0, 1), b2 + hstepB, vB0, vB1); PG8_STAGE(PG8_SA(0, 0), a2, cA00, cA01);
;             PG8_WAIT_V(8); PG8_WAIT_L(0); PG8_BAR; PG8_MMA(1, 0, At, B0); PG8_MMA(1, 1, At, B1); PG8_BAR; PG8_SCHED;
.LBB0_1433:
	s_ashr_i32 s17, s16, 31
	s_lshl_b64 s[40:41], s[16:17], 20
	s_add_u32 s40, s58, s40
	s_addc_u32 s41, s59, s41
	s_and_b64 s[42:43], s[36:37], exec
	s_cselect_b32 s17, s41, s11
	s_cselect_b32 s52, s40, s10
	s_ashr_i32 s35, s34, 31
	s_lshl_b64 s[42:43], s[34:35], 20
	s_add_u32 s42, s60, s42
	s_addc_u32 s43, s61, s43
	s_and_b64 s[48:49], s[36:37], exec
	s_cselect_b32 s35, s43, s47
	s_cselect_b32 s53, s42, s46
	s_add_u32 s54, s46, 0x100
	v_mov_b32_e32 v0, 0
	s_addc_u32 s55, s47, 0
	s_mov_b32 s87, -2
	ds_read_b128 v[146:149], v240
	ds_read_b128 v[150:153], v240 offset:1024
	ds_read_b128 v[154:157], v240 offset:2048
	ds_read_b128 v[158:161], v240 offset:3072
	ds_read_b128 v[162:165], v241
	ds_read_b128 v[166:169], v241 offset:1024
	ds_read_b128 v[170:173], v241 offset:2048
	ds_read_b128 v[174:177], v241 offset:3072
	s_add_u32 s46, s10, 0x100
	s_addc_u32 s47, s11, 0
	s_cmp_eq_u32 s87, 28
	s_cselect_b32 s51, s17, s47
	s_cselect_b32 s50, s52, s46
	s_cselect_b32 s49, s35, s55
	s_cselect_b32 s48, s53, s54
	v_lshl_add_u64 v[210:211], s[10:11], 0, v[142:143]
	s_add_i32 m0, s62, 0xc000
	ds_read_b128 v[178:181], v242
	ds_read_b128 v[182:185], v242 offset:1024
	ds_read_b128 v[186:189], v242 offset:2048
	ds_read_b128 v[190:193], v242 offset:3072
	ds_read_b128 v[194:197], v242 offset:4096
	ds_read_b128 v[198:201], v242 offset:5120
	ds_read_b128 v[202:205], v242 offset:6144
	ds_read_b128 v[206:209], v242 offset:7168
	global_load_lds_dwordx4 v[210:211], off
	v_lshl_add_u64 v[210:211], s[10:11], 0, v[140:141]
	s_add_i32 m0, s62, 0xe000
	s_nop 0
	global_load_lds_dwordx4 v[210:211], off
	s_waitcnt vmcnt(8)
	s_waitcnt lgkmcnt(0)
	s_barrier
	s_setprio 1
	s_waitcnt lgkmcnt(0)
	v_mfma_f32_16x16x32_bf16 v[124:127], v[146:149], v[178:181], 0
	v_mfma_f32_16x16x32_bf16 v[120:123], v[154:157], v[178:181], 0
	v_mfma_f32_16x16x32_bf16 v[116:119], v[146:149], v[186:189], 0
	v_mfma_f32_16x16x32_bf16 v[112:115], v[154:157], v[186:189], 0
	v_mfma_f32_16x16x32_bf16 v[108:111], v[146:149], v[194:197], 0
	v_mfma_f32_16x16x32_bf16 v[100:103], v[154:157], v[194:197], 0
	v_mfma_f32_16x16x32_bf16 v[92:95], v[146:149], v[202:205], 0
	v_mfma_f32_16x16x32_bf16 v[84:87], v[154:157], v[202:205], 0
	v_mfma_f32_16x16x32_bf16 v[124:127], v[150:153], v[182:185], v[124:127]
	v_mfma_f32_16x16x32_bf16 v[120:123], v[158:161], v[182:185], v[120:123]
	v_mfma_f32_16x16x32_bf16 v[116:119], v[150:153], v[190:193], v[116:119]
	v_mfma_f32_16x16x32_bf16 v[112:115], v[158:161], v[190:193], v[112:115]
	v_mfma_f32_16x16x32_bf16 v[108:111], v[150:153], v[198:201], v[108:111]
	v_mfma_f32_16x16x32_bf16 v[100:103], v[158:161], v[198:201], v[100:103]
	v_mfma_f32_16x16x32_bf16 v[92:95], v[150:153], v[206:209], v[92:95]
	v_mfma_f32_16x16x32_bf16 v[84:87], v[158:161], v[206:209], v[84:87]
	s_setprio 0
	s_setprio 1
	v_mfma_f32_16x16x32_bf16 v[104:107], v[162:165], v[178:181], 0
	v_mfma_f32_16x16x32_bf16 v[96:99], v[170:173], v[178:181], 0
	v_mfma_f32_16x16x32_bf16 v[88:91], v[162:165], v[186:189], 0
	v_mfma_f32_16x16x32_bf16 v[80:83], v[170:173], v[186:189], 0
	v_mfma_f32_16x16x32_bf16 v[76:79], v[162:165], v[194:197], 0
	v_mfma_f32_16x16x32_bf16 v[72:75], v[170:173], v[194:197], 0
	v_mfma_f32_16x16x32_bf16 v[68:71], v[162:165], v[202:205], 0
	v_mfma_f32_16x16x32_bf16 v[64:67], v[170:173], v[202:205], 0
	v_mfma_f32_16x16x32_bf16 v[104:107], v[166:169], v[182:185], v[104:107]
	v_mfma_f32_16x16x32_bf16 v[96:99], v[174:177], v[182:185], v[96:99]
	v_mfma_f32_16x16x32_bf16 v[88:91], v[166:169], v[190:193], v[88:91]
	v_mfma_f32_16x16x32_bf16 v[80:83], v[174:177], v[190:193], v[80:83]
	v_mfma_f32_16x16x32_bf16 v[76:79], v[166:169], v[198:201], v[76:79]
	v_mfma_f32_16x16x32_bf16 v[72:75], v[174:177], v[198:201], v[72:75]
	v_mfma_f32_16x16x32_bf16 v[68:71], v[166:169], v[206:209], v[68:71]
	v_mfma_f32_16x16x32_bf16 v[64:67], v[174:177], v[206:209], v[64:67]
	s_setprio 0
	s_barrier
	s_add_i32 s10, s80, s97
	v_lshl_add_u64 v[210:211], s[48:49], 0, v[128:129]
	s_mov_b32 m0, s10
	ds_read_b128 v[178:181], v242 offset:16384
	ds_read_b128 v[182:185], v242 offset:17408
	ds_read_b128 v[186:189], v242 offset:18432
	ds_read_b128 v[190:193], v242 offset:19456
	ds_read_b128 v[194:197], v242 offset:20480
	ds_read_b128 v[198:201], v242 offset:21504
	ds_read_b128 v[202:205], v242 offset:22528
	ds_read_b128 v[206:209], v242 offset:23552
	global_load_lds_dwordx4 v[210:211], off
	s_add_i32 m0, s10, 0x2000
	s_add_u32 s10, s48, 0x80000
	v_lshl_add_u64 v[212:213], s[48:49], 0, v[130:131]
	s_addc_u32 s11, s49, 0
	s_add_i32 s88, s81, s97
	global_load_lds_dwordx4 v[212:213], off
	v_lshl_add_u64 v[214:215], s[10:11], 0, v[128:129]
	s_mov_b32 m0, s88
	v_lshl_add_u64 v[216:217], s[50:51], 0, v[136:137]
	global_load_lds_dwordx4 v[214:215], off
	v_lshl_add_u64 v[214:215], s[10:11], 0, v[130:131]
	s_add_i32 m0, s88, 0x2000
	s_nop 0
	global_load_lds_dwordx4 v[214:215], off
	v_lshl_add_u64 v[214:215], s[50:51], 0, v[132:133]
	s_mov_b32 m0, s62
	s_nop 0
	global_load_lds_dwordx4 v[214:215], off
	s_mov_b32 m0, s63
	s_nop 0
	global_load_lds_dwordx4 v[216:217], off
	s_waitcnt vmcnt(8)
	s_waitcnt lgkmcnt(0)
	s_barrier
; #define PG8_STAGE(bufoff, gbase, o0, o1) do { \
;         __builtin_amdgcn_global_load_lds((const unsigned*)((const char*)(gbase) + (o0)), (LAS unsigned*)(lds + (bufoff) + ldsw), 16, 0, 0); \
;         __builtin_amdgcn_global_load_lds((const unsigned*)((const char*)(gbase) + (o1)), (LAS unsigned*)(lds + (bufoff) + ldsw + 8192), 16, 0, 0); } while (0)
; #define PG8_LDA(dst, b, h) do { _Pragma("unroll") for (int m = 0; m < 4; ++m) _Pragma("unroll") for (int k = 0; k < 2; ++k) dst[m][k] = *(const LAS bf16x8*)(lds + PG8_SA(b, h) + aoff + m * 2048 + k * 1024); } while (0)
; #define PG8_LDB(dst, b, h) do { _Pragma("unroll") for (int n = 0; n < 2; ++n) _Pragma("unroll") for (int k = 0; k < 2; ++k) dst[n][k] = *(const LAS bf16x8*)(lds + PG8_SB(b, h) + boff + n * 2048 + k * 1024); } while (0)
; #define PG8_WAIT_V(n) asm volatile("s_waitcnt vmcnt(" #n ")" ::: "memory")
; #define PG8_WAIT_L(n) asm volatile("s_waitcnt lgkmcnt(" #n ")" ::: "memory")
; #define PG8_BAR __builtin_amdgcn_s_barrier()
; #define PG8_SCHED __builtin_amdgcn_sched_barrier(0)
; template <class Epi, class Sched, class Prob>
; __device__ __forceinline__ void gemm_phase(LAS unsigned char* lds, LAS unsigned char* lds_epi, const Prob g, const Sched& S, const Epi& E, int wid) {
;     ...
;             PG8_WAIT_V(8); PG8_WAIT_L(0); PG8_BAR; PG8_MMA(1, 0, At, B0); PG8_MMA(1, 1, At, B1); PG8_BAR; PG8_SCHED;
;             PG8_LDB(B0, 1, 0); PG8_LDB(B1, 1, 1); PG8_SCHED; PG8_LDA(At, 1, 0); PG8_STAGE(PG8_SA(0, 1), a2, cA10, cA11);
;             PG8_WAIT_V(8); PG8_WAIT_L(0); PG8_BAR; PG8_MMA(0, 0, At, B0); PG8_MMA(0, 1, At, B1); PG8_BAR; PG8_SCHED;
	s_setprio 1
	s_waitcnt lgkmcnt(0)
	v_mfma_f32_16x16x32_bf16 v[60:63], v[146:149], v[178:181], 0
	v_mfma_f32_16x16x32_bf16 v[56:59], v[154:157], v[178:181], 0
	v_mfma_f32_16x16x32_bf16 v[52:55], v[146:149], v[186:189], 0
	v_mfma_f32_16x16x32_bf16 v[48:51], v[154:157], v[186:189], 0
	v_mfma_f32_16x16x32_bf16 v[36:39], v[146:149], v[194:197], 0
	v_mfma_f32_16x16x32_bf16 v[32:35], v[154:157], v[194:197], 0
	v_mfma_f32_16x16x32_bf16 v[20:23], v[146:149], v[202:205], 0
	v_mfma_f32_16x16x32_bf16 v[16:19], v[154:157], v[202:205], 0
	v_mfma_f32_16x16x32_bf16 v[60:63], v[150:153], v[182:185], v[60:63]
	v_mfma_f32_16x16x32_bf16 v[56:59], v[158:161], v[182:185], v[56:59]
	v_mfma_f32_16x16x32_bf16 v[52:55], v[150:153], v[190:193], v[52:55]
	v_mfma_f32_16x16x32_bf16 v[48:51], v[158:161], v[190:193], v[48:51]
	v_mfma_f32_16x16x32_bf16 v[36:39], v[150:153], v[198:201], v[36:39]
	v_mfma_f32_16x16x32_bf16 v[32:35], v[158:161], v[198:201], v[32:35]
	v_mfma_f32_16x16x32_bf16 v[20:23], v[150:153], v[206:209], v[20:23]
	v_mfma_f32_16x16x32_bf16 v[16:19], v[158:161], v[206:209], v[16:19]
	s_setprio 0
	s_setprio 1
	v_mfma_f32_16x16x32_bf16 v[44:47], v[162:165], v[178:181], 0
	v_mfma_f32_16x16x32_bf16 v[40:43], v[170:173], v[178:181], 0
	v_mfma_f32_16x16x32_bf16 v[28:31], v[162:165], v[186:189], 0
	v_mfma_f32_16x16x32_bf16 v[24:27], v[170:173], v[186:189], 0
	v_mfma_f32_16x16x32_bf16 v[12:15], v[162:165], v[194:197], 0
	v_mfma_f32_16x16x32_bf16 v[8:11], v[170:173], v[194:197], 0
	v_mfma_f32_16x16x32_bf16 v[4:7], v[162:165], v[202:205], 0
	v_mfma_f32_16x16x32_bf16 v[0:3], v[170:173], v[202:205], 0
	v_mfma_f32_16x16x32_bf16 v[44:47], v[166:169], v[182:185], v[44:47]
	v_mfma_f32_16x16x32_bf16 v[40:43], v[174:177], v[182:185], v[40:43]
	v_mfma_f32_16x16x32_bf16 v[28:31], v[166:169], v[190:193], v[28:31]
	v_mfma_f32_16x16x32_bf16 v[24:27], v[174:177], v[190:193], v[24:27]
	v_mfma_f32_16x16x32_bf16 v[12:15], v[166:169], v[198:201], v[12:15]
	v_mfma_f32_16x16x32_bf16 v[8:11], v[174:177], v[198:201], v[8:11]
	v_mfma_f32_16x16x32_bf16 v[4:7], v[166:169], v[206:209], v[4:7]
	v_mfma_f32_16x16x32_bf16 v[0:3], v[174:177], v[206:209], v[0:3]
	s_setprio 0
	s_barrier
	s_add_i32 s10, 0, 0x18000
	s_add_i32 s88, 0, 0x1c000
	v_add_u32_e32 v158, s10, v239
	v_add_u32_e32 v174, s88, v239
	ds_read_b128 v[146:149], v158
	ds_read_b128 v[150:153], v158 offset:1024
	ds_read_b128 v[154:157], v158 offset:2048
	ds_read_b128 v[158:161], v158 offset:3072
	ds_read_b128 v[162:165], v174
	ds_read_b128 v[166:169], v174 offset:1024
	ds_read_b128 v[170:173], v174 offset:2048
	ds_read_b128 v[174:177], v174 offset:3072
	s_mov_b32 m0, s64
	v_lshl_add_u64 v[218:219], s[50:51], 0, v[134:135]
	ds_read_b128 v[178:181], v242 offset:32768
	ds_read_b128 v[182:185], v242 offset:33792
	ds_read_b128 v[186:189], v242 offset:34816
	ds_read_b128 v[190:193], v242 offset:35840
	ds_read_b128 v[194:197], v242 offset:36864
	ds_read_b128 v[198:201], v242 offset:37888
	ds_read_b128 v[202:205], v242 offset:38912
	ds_read_b128 v[206:209], v242 offset:39936
	global_load_lds_dwordx4 v[218:219], off
	v_lshl_add_u64 v[218:219], s[50:51], 0, v[138:139]
	s_mov_b32 m0, s65
	s_nop 0
	global_load_lds_dwordx4 v[218:219], off
	s_waitcnt vmcnt(8)
	s_waitcnt lgkmcnt(0)
	s_barrier
	s_setprio 1
	s_waitcnt lgkmcnt(0)
	v_mfma_f32_16x16x32_bf16 v[124:127], v[146:149], v[178:181], v[124:127]
	v_mfma_f32_16x16x32_bf16 v[120:123], v[154:157], v[178:181], v[120:123]
	v_mfma_f32_16x16x32_bf16 v[116:119], v[146:149], v[186:189], v[116:119]
	v_mfma_f32_16x16x32_bf16 v[112:115], v[154:157], v[186:189], v[112:115]
	v_mfma_f32_16x16x32_bf16 v[108:111], v[146:149], v[194:197], v[108:111]
	v_mfma_f32_16x16x32_bf16 v[100:103], v[154:157], v[194:197], v[100:103]
	v_mfma_f32_16x16x32_bf16 v[92:95], v[146:149], v[202:205], v[92:95]
	v_mfma_f32_16x16x32_bf16 v[84:87], v[154:157], v[202:205], v[84:87]
	v_mfma_f32_16x16x32_bf16 v[124:127], v[150:153], v[182:185], v[124:127]
	v_mfma_f32_16x16x32_bf16 v[120:123], v[158:161], v[182:185], v[120:123]
	v_mfma_f32_16x16x32_bf16 v[116:119], v[150:153], v[190:193], v[116:119]
	v_mfma_f32_16x16x32_bf16 v[112:115], v[158:161], v[190:193], v[112:115]
	v_mfma_f32_16x16x32_bf16 v[108:111], v[150:153], v[198:201], v[108:111]
	v_mfma_f32_16x16x32_bf16 v[100:103], v[158:161], v[198:201], v[100:103]
	v_mfma_f32_16x16x32_bf16 v[92:95], v[150:153], v[206:209], v[92:95]
	v_mfma_f32_16x16x32_bf16 v[84:87], v[158:161], v[206:209], v[84:87]
	s_setprio 0
	s_setprio 1
	v_mfma_f32_16x16x32_bf16 v[104:107], v[162:165], v[178:181], v[104:107]
	v_mfma_f32_16x16x32_bf16 v[96:99], v[170:173], v[178:181], v[96:99]
	v_mfma_f32_16x16x32_bf16 v[88:91], v[162:165], v[186:189], v[88:91]
	v_mfma_f32_16x16x32_bf16 v[80:83], v[170:173], v[186:189], v[80:83]
	v_mfma_f32_16x16x32_bf16 v[76:79], v[162:165], v[194:197], v[76:79]
	v_mfma_f32_16x16x32_bf16 v[72:75], v[170:173], v[194:197], v[72:75]
	v_mfma_f32_16x16x32_bf16 v[68:71], v[162:165], v[202:205], v[68:71]
	v_mfma_f32_16x16x32_bf16 v[64:67], v[170:173], v[202:205], v[64:67]
	v_mfma_f32_16x16x32_bf16 v[104:107], v[166:169], v[182:185], v[104:107]
	v_mfma_f32_16x16x32_bf16 v[96:99], v[174:177], v[182:185], v[96:99]
	v_mfma_f32_16x16x32_bf16 v[88:91], v[166:169], v[190:193], v[88:91]
	v_mfma_f32_16x16x32_bf16 v[80:83], v[174:177], v[190:193], v[80:83]
	v_mfma_f32_16x16x32_bf16 v[76:79], v[166:169], v[198:201], v[76:79]
	v_mfma_f32_16x16x32_bf16 v[72:75], v[174:177], v[198:201], v[72:75]
	v_mfma_f32_16x16x32_bf16 v[68:71], v[166:169], v[206:209], v[68:71]
	v_mfma_f32_16x16x32_bf16 v[64:67], v[174:177], v[206:209], v[64:67]
	s_setprio 0
	s_barrier
; #define PG8_STAGE(bufoff, gbase, o0, o1) do { \
;         __builtin_amdgcn_global_load_lds((const unsigned*)((const char*)(gbase) + (o0)), (LAS unsigned*)(lds + (bufoff) + ldsw), 16, 0, 0); \
;         __builtin_amdgcn_global_load_lds((const unsigned*)((const char*)(gbase) + (o1)), (LAS unsigned*)(lds + (bufoff) + ldsw + 8192), 16, 0, 0); } while (0)
; #define PG8_LDA(dst, b, h) do { _Pragma("unroll") for (int m = 0; m < 4; ++m) _Pragma("unroll") for (int k = 0; k < 2; ++k) dst[m][k] = *(const LAS bf16x8*)(lds + PG8_SA(b, h) + aoff + m * 2048 + k * 1024); } while (0)
; #define PG8_WAIT_V(n) asm volatile("s_waitcnt vmcnt(" #n ")" ::: "memory")
; #define PG8_WAIT_L(n) asm volatile("s_waitcnt lgkmcnt(" #n ")" ::: "memory")
; #define PG8_BAR __builtin_amdgcn_s_barrier()
; #define PG8_SCHED __builtin_amdgcn_sched_barrier(0)
; template <class Epi, class Sched, class Prob>
; __device__ __forceinline__ void gemm_phase(LAS unsigned char* lds, LAS unsigned char* lds_epi, const Prob g, const Sched& S, const Epi& E, int wid) {
;     ...
;             PG8_LDA(At, 1, 1); PG8_STAGE(PG8_SB(1, 0), b3, vB0, vB1); PG8_STAGE(PG8_SB(1, 1), b3 + hstepB, vB0, vB1); PG8_STAGE(PG8_SA(1, 0), a3, cA00, cA01);
;             PG8_WAIT_V(8); PG8_WAIT_L(0); PG8_BAR; PG8_MMA(1, 0, At, B0); PG8_MMA(1, 1, At, B1); PG8_BAR; PG8_SCHED;
	s_add_i32 s10, s10, s97
	v_lshl_add_u64 v[210:211], v[210:211], 0, s[24:25]
	s_mov_b32 m0, s10
	ds_read_b128 v[178:181], v242 offset:49152
	ds_read_b128 v[182:185], v242 offset:50176
	ds_read_b128 v[186:189], v242 offset:51200
	ds_read_b128 v[190:193], v242 offset:52224
	ds_read_b128 v[194:197], v242 offset:53248
	ds_read_b128 v[198:201], v242 offset:54272
	ds_read_b128 v[202:205], v242 offset:55296
	ds_read_b128 v[206:209], v242 offset:56320
	global_load_lds_dwordx4 v[210:211], off
	s_add_i32 m0, s10, 0x2000
	s_add_u32 s10, s48, 0x80080
	v_lshl_add_u64 v[210:211], v[212:213], 0, s[24:25]
	s_addc_u32 s11, s49, 0
	s_add_i32 s48, s88, s97
	global_load_lds_dwordx4 v[210:211], off
	v_lshl_add_u64 v[210:211], s[10:11], 0, v[128:129]
	s_mov_b32 m0, s48
	s_nop 0
	global_load_lds_dwordx4 v[210:211], off
	v_lshl_add_u64 v[210:211], s[10:11], 0, v[130:131]
	s_add_i32 m0, s48, 0x2000
	s_nop 0
	global_load_lds_dwordx4 v[210:211], off
	v_lshl_add_u64 v[210:211], v[214:215], 0, s[24:25]
	s_mov_b32 m0, s78
	s_nop 0
	global_load_lds_dwordx4 v[210:211], off
	v_lshl_add_u64 v[210:211], v[216:217], 0, s[24:25]
	s_mov_b32 m0, s79
	s_nop 0
	global_load_lds_dwordx4 v[210:211], off
	s_waitcnt vmcnt(8)
	s_waitcnt lgkmcnt(0)
	s_barrier
	s_setprio 1
	s_waitcnt lgkmcnt(0)
	v_mfma_f32_16x16x32_bf16 v[60:63], v[146:149], v[178:181], v[60:63]
	v_mfma_f32_16x16x32_bf16 v[56:59], v[154:157], v[178:181], v[56:59]
	v_mfma_f32_16x16x32_bf16 v[52:55], v[146:149], v[186:189], v[52:55]
	v_mfma_f32_16x16x32_bf16 v[48:51], v[154:157], v[186:189], v[48:51]
	v_mfma_f32_16x16x32_bf16 v[36:39], v[146:149], v[194:197], v[36:39]
	v_mfma_f32_16x16x32_bf16 v[32:35], v[154:157], v[194:197], v[32:35]
	v_mfma_f32_16x16x32_bf16 v[20:23], v[146:149], v[202:205], v[20:23]
	v_mfma_f32_16x16x32_bf16 v[16:19], v[154:157], v[202:205], v[16:19]
	v_mfma_f32_16x16x32_bf16 v[60:63], v[150:153], v[182:185], v[60:63]
	v_mfma_f32_16x16x32_bf16 v[56:59], v[158:161], v[182:185], v[56:59]
	v_mfma_f32_16x16x32_bf16 v[52:55], v[150:153], v[190:193], v[52:55]
	v_mfma_f32_16x16x32_bf16 v[48:51], v[158:161], v[190:193], v[48:51]
	v_mfma_f32_16x16x32_bf16 v[36:39], v[150:153], v[198:201], v[36:39]
	v_mfma_f32_16x16x32_bf16 v[32:35], v[158:161], v[198:201], v[32:35]
	v_mfma_f32_16x16x32_bf16 v[20:23], v[150:153], v[206:209], v[20:23]
	v_mfma_f32_16x16x32_bf16 v[16:19], v[158:161], v[206:209], v[16:19]
	s_setprio 0
	s_setprio 1
	v_mfma_f32_16x16x32_bf16 v[44:47], v[162:165], v[178:181], v[44:47]
	v_mfma_f32_16x16x32_bf16 v[40:43], v[170:173], v[178:181], v[40:43]
	v_mfma_f32_16x16x32_bf16 v[28:31], v[162:165], v[186:189], v[28:31]
	v_mfma_f32_16x16x32_bf16 v[24:27], v[170:173], v[186:189], v[24:27]
	v_mfma_f32_16x16x32_bf16 v[12:15], v[162:165], v[194:197], v[12:15]
	v_mfma_f32_16x16x32_bf16 v[8:11], v[170:173], v[194:197], v[8:11]
	v_mfma_f32_16x16x32_bf16 v[4:7], v[162:165], v[202:205], v[4:7]
	v_mfma_f32_16x16x32_bf16 v[0:3], v[170:173], v[202:205], v[0:3]
	v_mfma_f32_16x16x32_bf16 v[44:47], v[166:169], v[182:185], v[44:47]
	v_mfma_f32_16x16x32_bf16 v[40:43], v[174:177], v[182:185], v[40:43]
	v_mfma_f32_16x16x32_bf16 v[28:31], v[166:169], v[190:193], v[28:31]
	v_mfma_f32_16x16x32_bf16 v[24:27], v[174:177], v[190:193], v[24:27]
	v_mfma_f32_16x16x32_bf16 v[12:15], v[166:169], v[198:201], v[12:15]
	v_mfma_f32_16x16x32_bf16 v[8:11], v[174:177], v[198:201], v[8:11]
	v_mfma_f32_16x16x32_bf16 v[4:7], v[166:169], v[206:209], v[4:7]
	v_mfma_f32_16x16x32_bf16 v[0:3], v[174:177], v[206:209], v[0:3]
	s_setprio 0
	s_barrier
	s_add_i32 s87, s87, 2
	s_add_u32 s54, s54, 0x100
	s_addc_u32 s55, s55, 0
	s_cmp_gt_u32 s87, 29
	s_mov_b64 s[10:11], s[46:47]

; #define PG8_STAGE(bufoff, gbase, o0, o1) do { \
;         __builtin_amdgcn_global_load_lds((const unsigned*)((const char*)(gbase) + (o0)), (LAS unsigned*)(lds + (bufoff) + ldsw), 16, 0, 0); \
;         __builtin_amdgcn_global_load_lds((const unsigned*)((const char*)(gbase) + (o1)), (LAS unsigned*)(lds + (bufoff) + ldsw + 8192), 16, 0, 0); } while (0)
; #define PG8_LDA(dst, b, h) do { _Pragma("unroll") for (int m = 0; m < 4; ++m) _Pragma("unroll") for (int k = 0; k < 2; ++k) dst[m][k] = *(const LAS bf16x8*)(lds + PG8_SA(b, h) + aoff + m * 2048 + k * 1024); } while (0)
; #define PG8_LDB(dst, b, h) do { _Pragma("unroll") for (int n = 0; n < 2; ++n) _Pragma("unroll") for (int k = 0; k < 2; ++k) dst[n][k] = *(const LAS bf16x8*)(lds + PG8_SB(b, h) + boff + n * 2048 + k * 1024); } while (0)
; #define PG8_WAIT_V(n) asm volatile("s_waitcnt vmcnt(" #n ")" ::: "memory")
; #define PG8_WAIT_L(n) asm volatile("s_waitcnt lgkmcnt(" #n ")" ::: "memory")
; #define PG8_BAR __builtin_amdgcn_s_barrier()
; #define PG8_SCHED __builtin_amdgcn_sched_barrier(0)
; template <class Epi, class Sched, class Prob>
; __device__ __forceinline__ void gemm_phase(LAS unsigned char* lds, LAS unsigned char* lds_epi, const Prob g, const Sched& S, const Epi& E, int wid) {
;     ...
;         const bool has_next = S.next(ui + 1, nxt);
;         const char* nA = has_next ? g.a_base(nxt) : cA; const char* nB = has_next ? g.b_base(nxt) : cB;
; _Pragma("clang loop unroll(disable)")
;         for (int t = 0; t < nt; t += 2) {
;             const bool last = (t == nt - 2);
;             const char* a1 = cA + (size_t)(t + 1) * kstep;
;             const char* a2 = last ? nA : cA + (size_t)(t + 2) * kstep; const char* b2 = last ? nB : cB + (size_t)(t + 2) * kstep;
;             const char* a3 = a2 + kstep; const char* b3 = b2 + kstep;
;             PG8_LDB(B0, 0, 0); PG8_LDB(B1, 0, 1); PG8_SCHED; PG8_LDA(At, 0, 0); PG8_STAGE(PG8_SA(1, 1), a1, cA10, cA11);
;             PG8_WAIT_V(8); PG8_WAIT_L(0); PG8_BAR; PG8_MMA(0, 0, At, B0); PG8_MMA(0, 1, At, B1); PG8_BAR; PG8_SCHED;
;             PG8_LDA(At, 0, 1); PG8_STAGE(PG8_SB(0, 0), b2, vB0, vB1); PG8_STAGE(PG8_SB(0, 1), b2 + hstepB, vB0, vB1); PG8_STAGE(PG8_SA(0, 0), a2, cA00, cA01);
;             PG8_WAIT_V(8); PG8_WAIT_L(0); PG8_BAR; PG8_MMA(1, 0, At, B0); PG8_MMA(1, 1, At, B1); PG8_BAR; PG8_SCHED;
.LBB0_1594:
	s_ashr_i32 s65, s64, 31
	s_lshl_b64 s[14:15], s[64:65], 20
	s_add_u32 s17, s40, s14
	s_addc_u32 s19, s41, s15
	s_ashr_i32 s14, s62, 1
	s_ashr_i32 s15, s14, 31
	s_lshl_b64 s[14:15], s[14:15], 9
	s_add_u32 s68, s17, s14
	s_addc_u32 s69, s19, s15
	s_and_b64 s[14:15], s[66:67], exec
	s_cselect_b32 s17, s69, s9
	s_cselect_b32 s19, s68, s8
	s_ashr_i32 s63, s62, 31
	s_lshl_b64 s[14:15], s[62:63], 17
	s_add_u32 s70, s33, s14
	s_addc_u32 s71, s76, s15
	s_and_b64 s[14:15], s[66:67], exec
	v_mov_b32_e32 v0, 0
	s_cselect_b32 s26, s71, s11
	s_cselect_b32 s27, s70, s10
	s_mov_b64 s[20:21], -1
	s_mov_b64 s[14:15], 0
	s_add_u32 s24, s8, s14
	s_addc_u32 s25, s9, s15
	s_add_u32 s22, s24, 0x100
	s_addc_u32 s23, s25, 0
	v_cndmask_b32_e64 v56, 0, 1, s[20:21]
	s_and_b64 s[20:21], s[12:13], exec
	s_cselect_b32 s20, s19, s22
	s_cselect_b32 s21, s17, s23
	s_add_u32 s14, s10, s14
	s_addc_u32 s15, s11, s15
	s_add_u32 s14, s14, 0x100
	v_cmp_ne_u32_e32 vcc, 1, v56
	ds_read_b128 v[56:59], v221
	ds_read_b128 v[68:71], v221 offset:1024
	ds_read_b128 v[72:75], v221 offset:2048
	ds_read_b128 v[88:91], v221 offset:3072
	ds_read_b128 v[100:103], v222
	ds_read_b128 v[104:107], v222 offset:1024
	ds_read_b128 v[166:169], v222 offset:2048
	ds_read_b128 v[170:173], v222 offset:3072
	s_addc_u32 s15, s15, 0
	s_and_b64 s[12:13], s[12:13], exec
	s_cselect_b32 s15, s26, s15
	s_cselect_b32 s14, s27, s14
	s_add_i32 s65, s85, s97
	s_add_i32 m0, s77, 0xc000
	s_add_i32 s72, s77, 0xe000
	s_add_i32 s36, s65, 0x2000
	s_add_u32 s22, s14, 0x10000
	s_addc_u32 s23, s15, 0
	s_add_i32 s35, 0, 0x18000
	s_add_i32 s63, s86, s97
	s_add_i32 s31, s35, s97
	s_add_i32 s37, s63, 0x2000
	s_add_i32 s34, 0, 0x1c000
	s_add_i32 s29, s31, 0x2000
	s_add_u32 s12, s14, 0x10080
	s_addc_u32 s13, s15, 0
	s_add_i32 s30, s34, s97
	s_add_i32 s28, s30, 0x2000
	v_lshl_add_u64 v[206:207], s[24:25], 0, v[158:159]
	v_lshl_add_u64 v[206:207], v[206:207], 0, s[54:55]
	ds_read_b128 v[174:177], v223
	ds_read_b128 v[178:181], v223 offset:1024
	ds_read_b128 v[182:185], v223 offset:2048
	ds_read_b128 v[186:189], v223 offset:3072
	ds_read_b128 v[190:193], v223 offset:4096
	ds_read_b128 v[194:197], v223 offset:5120
	ds_read_b128 v[198:201], v223 offset:6144
	ds_read_b128 v[202:205], v223 offset:7168
	global_load_lds_dwordx4 v[206:207], off
	v_lshl_add_u64 v[206:207], s[24:25], 0, v[162:163]
	v_lshl_add_u64 v[206:207], v[206:207], 0, s[54:55]
	s_mov_b32 m0, s72
	s_nop 0
	global_load_lds_dwordx4 v[206:207], off
	s_waitcnt vmcnt(8)
	s_waitcnt lgkmcnt(0)
	s_barrier
	s_setprio 1
	s_waitcnt lgkmcnt(0)
	v_mfma_f32_16x16x32_bf16 v[148:151], v[56:59], v[174:177], 0
	v_mfma_f32_16x16x32_bf16 v[116:119], v[72:75], v[174:177], 0
	v_mfma_f32_16x16x32_bf16 v[144:147], v[56:59], v[182:185], 0
	v_mfma_f32_16x16x32_bf16 v[112:115], v[72:75], v[182:185], 0
	v_mfma_f32_16x16x32_bf16 v[140:143], v[56:59], v[190:193], 0
	v_mfma_f32_16x16x32_bf16 v[108:111], v[72:75], v[190:193], 0
	v_mfma_f32_16x16x32_bf16 v[136:139], v[56:59], v[198:201], 0
	v_mfma_f32_16x16x32_bf16 v[96:99], v[72:75], v[198:201], 0
	v_mfma_f32_16x16x32_bf16 v[148:151], v[68:71], v[178:181], v[148:151]
	v_mfma_f32_16x16x32_bf16 v[116:119], v[88:91], v[178:181], v[116:119]
	v_mfma_f32_16x16x32_bf16 v[144:147], v[68:71], v[186:189], v[144:147]
	v_mfma_f32_16x16x32_bf16 v[112:115], v[88:91], v[186:189], v[112:115]
	v_mfma_f32_16x16x32_bf16 v[140:143], v[68:71], v[194:197], v[140:143]
	v_mfma_f32_16x16x32_bf16 v[108:111], v[88:91], v[194:197], v[108:111]
	v_mfma_f32_16x16x32_bf16 v[136:139], v[68:71], v[202:205], v[136:139]
	v_mfma_f32_16x16x32_bf16 v[96:99], v[88:91], v[202:205], v[96:99]
	s_setprio 0
	s_setprio 1
	v_mfma_f32_16x16x32_bf16 v[132:135], v[100:103], v[174:177], 0
	v_mfma_f32_16x16x32_bf16 v[92:95], v[166:169], v[174:177], 0
	v_mfma_f32_16x16x32_bf16 v[128:131], v[100:103], v[182:185], 0
	v_mfma_f32_16x16x32_bf16 v[84:87], v[166:169], v[182:185], 0
	v_mfma_f32_16x16x32_bf16 v[124:127], v[100:103], v[190:193], 0
	v_mfma_f32_16x16x32_bf16 v[80:83], v[166:169], v[190:193], 0
	v_mfma_f32_16x16x32_bf16 v[120:123], v[100:103], v[198:201], 0
	v_mfma_f32_16x16x32_bf16 v[76:79], v[166:169], v[198:201], 0
	v_mfma_f32_16x16x32_bf16 v[132:135], v[104:107], v[178:181], v[132:135]
	v_mfma_f32_16x16x32_bf16 v[92:95], v[170:173], v[178:181], v[92:95]
	v_mfma_f32_16x16x32_bf16 v[128:131], v[104:107], v[186:189], v[128:131]
	v_mfma_f32_16x16x32_bf16 v[84:87], v[170:173], v[186:189], v[84:87]
	v_mfma_f32_16x16x32_bf16 v[124:127], v[104:107], v[194:197], v[124:127]
	v_mfma_f32_16x16x32_bf16 v[80:83], v[170:173], v[194:197], v[80:83]
	v_mfma_f32_16x16x32_bf16 v[120:123], v[104:107], v[202:205], v[120:123]
	v_mfma_f32_16x16x32_bf16 v[76:79], v[170:173], v[202:205], v[76:79]
	s_setprio 0
	s_barrier
	s_mov_b32 m0, s65
	v_lshl_add_u64 v[206:207], s[14:15], 0, v[152:153]
	ds_read_b128 v[174:177], v223 offset:16384
	ds_read_b128 v[178:181], v223 offset:17408
	ds_read_b128 v[182:185], v223 offset:18432
	ds_read_b128 v[186:189], v223 offset:19456
	ds_read_b128 v[190:193], v223 offset:20480
	ds_read_b128 v[194:197], v223 offset:21504
	ds_read_b128 v[198:201], v223 offset:22528
	ds_read_b128 v[202:205], v223 offset:23552
	global_load_lds_dwordx4 v[206:207], off
	v_lshl_add_u64 v[208:209], s[14:15], 0, v[154:155]
	s_mov_b32 m0, s36
	v_lshl_add_u64 v[210:211], s[22:23], 0, v[152:153]
	global_load_lds_dwordx4 v[208:209], off
	s_mov_b32 m0, s63
	v_lshl_add_u64 v[212:213], s[20:21], 0, v[160:161]
	global_load_lds_dwordx4 v[210:211], off
	v_lshl_add_u64 v[210:211], s[22:23], 0, v[154:155]
	s_mov_b32 m0, s37
	s_nop 0
	global_load_lds_dwordx4 v[210:211], off
	v_lshl_add_u64 v[210:211], s[20:21], 0, v[156:157]
	s_mov_b32 m0, s77
	s_nop 0
	global_load_lds_dwordx4 v[210:211], off
	s_mov_b32 m0, s78
	s_nop 0
	global_load_lds_dwordx4 v[212:213], off
	s_waitcnt vmcnt(8)
	s_waitcnt lgkmcnt(0)
	s_barrier
; #define PG8_STAGE(bufoff, gbase, o0, o1) do { \
;         __builtin_amdgcn_global_load_lds((const unsigned*)((const char*)(gbase) + (o0)), (LAS unsigned*)(lds + (bufoff) + ldsw), 16, 0, 0); \
;         __builtin_amdgcn_global_load_lds((const unsigned*)((const char*)(gbase) + (o1)), (LAS unsigned*)(lds + (bufoff) + ldsw + 8192), 16, 0, 0); } while (0)
; #define PG8_LDA(dst, b, h) do { _Pragma("unroll") for (int m = 0; m < 4; ++m) _Pragma("unroll") for (int k = 0; k < 2; ++k) dst[m][k] = *(const LAS bf16x8*)(lds + PG8_SA(b, h) + aoff + m * 2048 + k * 1024); } while (0)
; #define PG8_LDB(dst, b, h) do { _Pragma("unroll") for (int n = 0; n < 2; ++n) _Pragma("unroll") for (int k = 0; k < 2; ++k) dst[n][k] = *(const LAS bf16x8*)(lds + PG8_SB(b, h) + boff + n * 2048 + k * 1024); } while (0)
; #define PG8_WAIT_V(n) asm volatile("s_waitcnt vmcnt(" #n ")" ::: "memory")
; #define PG8_WAIT_L(n) asm volatile("s_waitcnt lgkmcnt(" #n ")" ::: "memory")
; #define PG8_BAR __builtin_amdgcn_s_barrier()
; #define PG8_SCHED __builtin_amdgcn_sched_barrier(0)
; template <class Epi, class Sched, class Prob>
; __device__ __forceinline__ void gemm_phase(LAS unsigned char* lds, LAS unsigned char* lds_epi, const Prob g, const Sched& S, const Epi& E, int wid) {
;     ...
;             PG8_WAIT_V(8); PG8_WAIT_L(0); PG8_BAR; PG8_MMA(1, 0, At, B0); PG8_MMA(1, 1, At, B1); PG8_BAR; PG8_SCHED;
;             PG8_LDB(B0, 1, 0); PG8_LDB(B1, 1, 1); PG8_SCHED; PG8_LDA(At, 1, 0); PG8_STAGE(PG8_SA(0, 1), a2, cA10, cA11);
;             PG8_WAIT_V(8); PG8_WAIT_L(0); PG8_BAR; PG8_MMA(0, 0, At, B0); PG8_MMA(0, 1, At, B1); PG8_BAR; PG8_SCHED;
	s_setprio 1
	s_waitcnt lgkmcnt(0)
	v_mfma_f32_16x16x32_bf16 v[64:67], v[56:59], v[174:177], 0
	v_mfma_f32_16x16x32_bf16 v[28:31], v[72:75], v[174:177], 0
	v_mfma_f32_16x16x32_bf16 v[60:63], v[56:59], v[182:185], 0
	v_mfma_f32_16x16x32_bf16 v[24:27], v[72:75], v[182:185], 0
	v_mfma_f32_16x16x32_bf16 v[52:55], v[56:59], v[190:193], 0
	v_mfma_f32_16x16x32_bf16 v[20:23], v[72:75], v[190:193], 0
	v_mfma_f32_16x16x32_bf16 v[48:51], v[56:59], v[198:201], 0
	v_mfma_f32_16x16x32_bf16 v[16:19], v[72:75], v[198:201], 0
	v_mfma_f32_16x16x32_bf16 v[64:67], v[68:71], v[178:181], v[64:67]
	v_mfma_f32_16x16x32_bf16 v[28:31], v[88:91], v[178:181], v[28:31]
	v_mfma_f32_16x16x32_bf16 v[60:63], v[68:71], v[186:189], v[60:63]
	v_mfma_f32_16x16x32_bf16 v[24:27], v[88:91], v[186:189], v[24:27]
	v_mfma_f32_16x16x32_bf16 v[52:55], v[68:71], v[194:197], v[52:55]
	v_mfma_f32_16x16x32_bf16 v[20:23], v[88:91], v[194:197], v[20:23]
	v_mfma_f32_16x16x32_bf16 v[48:51], v[68:71], v[202:205], v[48:51]
	v_mfma_f32_16x16x32_bf16 v[16:19], v[88:91], v[202:205], v[16:19]
	s_setprio 0
	s_setprio 1
	v_mfma_f32_16x16x32_bf16 v[44:47], v[100:103], v[174:177], 0
	v_mfma_f32_16x16x32_bf16 v[12:15], v[166:169], v[174:177], 0
	v_mfma_f32_16x16x32_bf16 v[40:43], v[100:103], v[182:185], 0
	v_mfma_f32_16x16x32_bf16 v[8:11], v[166:169], v[182:185], 0
	v_mfma_f32_16x16x32_bf16 v[36:39], v[100:103], v[190:193], 0
	v_mfma_f32_16x16x32_bf16 v[4:7], v[166:169], v[190:193], 0
	v_mfma_f32_16x16x32_bf16 v[32:35], v[100:103], v[198:201], 0
	v_mfma_f32_16x16x32_bf16 v[0:3], v[166:169], v[198:201], 0
	v_mfma_f32_16x16x32_bf16 v[44:47], v[104:107], v[178:181], v[44:47]
	v_mfma_f32_16x16x32_bf16 v[12:15], v[170:173], v[178:181], v[12:15]
	v_mfma_f32_16x16x32_bf16 v[40:43], v[104:107], v[186:189], v[40:43]
	v_mfma_f32_16x16x32_bf16 v[8:11], v[170:173], v[186:189], v[8:11]
	v_mfma_f32_16x16x32_bf16 v[36:39], v[104:107], v[194:197], v[36:39]
	v_mfma_f32_16x16x32_bf16 v[4:7], v[170:173], v[194:197], v[4:7]
	v_mfma_f32_16x16x32_bf16 v[32:35], v[104:107], v[202:205], v[32:35]
	v_mfma_f32_16x16x32_bf16 v[0:3], v[170:173], v[202:205], v[0:3]
	s_setprio 0
	s_barrier
	v_add_u32_e32 v88, s35, v220
	v_add_u32_e32 v170, s34, v220
	ds_read_b128 v[56:59], v88
	ds_read_b128 v[68:71], v88 offset:1024
	ds_read_b128 v[72:75], v88 offset:2048
	ds_read_b128 v[88:91], v88 offset:3072
	ds_read_b128 v[100:103], v170
	ds_read_b128 v[104:107], v170 offset:1024
	ds_read_b128 v[166:169], v170 offset:2048
	ds_read_b128 v[170:173], v170 offset:3072
	s_mov_b32 m0, s79
	v_lshl_add_u64 v[214:215], s[20:21], 0, v[158:159]
	ds_read_b128 v[174:177], v223 offset:32768
	ds_read_b128 v[178:181], v223 offset:33792
	ds_read_b128 v[182:185], v223 offset:34816
	ds_read_b128 v[186:189], v223 offset:35840
	ds_read_b128 v[190:193], v223 offset:36864
	ds_read_b128 v[194:197], v223 offset:37888
	ds_read_b128 v[198:201], v223 offset:38912
	ds_read_b128 v[202:205], v223 offset:39936
	global_load_lds_dwordx4 v[214:215], off
	v_lshl_add_u64 v[214:215], s[20:21], 0, v[162:163]
	s_mov_b32 m0, s80
	s_nop 0
	global_load_lds_dwordx4 v[214:215], off
	s_waitcnt vmcnt(8)
	s_waitcnt lgkmcnt(0)
	s_barrier
	s_setprio 1
	s_waitcnt lgkmcnt(0)
	v_mfma_f32_16x16x32_bf16 v[148:151], v[56:59], v[174:177], v[148:151]
	v_mfma_f32_16x16x32_bf16 v[116:119], v[72:75], v[174:177], v[116:119]
	v_mfma_f32_16x16x32_bf16 v[144:147], v[56:59], v[182:185], v[144:147]
	v_mfma_f32_16x16x32_bf16 v[112:115], v[72:75], v[182:185], v[112:115]
	v_mfma_f32_16x16x32_bf16 v[140:143], v[56:59], v[190:193], v[140:143]
	v_mfma_f32_16x16x32_bf16 v[108:111], v[72:75], v[190:193], v[108:111]
	v_mfma_f32_16x16x32_bf16 v[136:139], v[56:59], v[198:201], v[136:139]
	v_mfma_f32_16x16x32_bf16 v[96:99], v[72:75], v[198:201], v[96:99]
	v_mfma_f32_16x16x32_bf16 v[148:151], v[68:71], v[178:181], v[148:151]
	v_mfma_f32_16x16x32_bf16 v[116:119], v[88:91], v[178:181], v[116:119]
	v_mfma_f32_16x16x32_bf16 v[144:147], v[68:71], v[186:189], v[144:147]
	v_mfma_f32_16x16x32_bf16 v[112:115], v[88:91], v[186:189], v[112:115]
	v_mfma_f32_16x16x32_bf16 v[140:143], v[68:71], v[194:197], v[140:143]
	v_mfma_f32_16x16x32_bf16 v[108:111], v[88:91], v[194:197], v[108:111]
	v_mfma_f32_16x16x32_bf16 v[136:139], v[68:71], v[202:205], v[136:139]
	v_mfma_f32_16x16x32_bf16 v[96:99], v[88:91], v[202:205], v[96:99]
	s_setprio 0
	s_setprio 1
	v_mfma_f32_16x16x32_bf16 v[132:135], v[100:103], v[174:177], v[132:135]
	v_mfma_f32_16x16x32_bf16 v[92:95], v[166:169], v[174:177], v[92:95]
	v_mfma_f32_16x16x32_bf16 v[128:131], v[100:103], v[182:185], v[128:131]
	v_mfma_f32_16x16x32_bf16 v[84:87], v[166:169], v[182:185], v[84:87]
	v_mfma_f32_16x16x32_bf16 v[124:127], v[100:103], v[190:193], v[124:127]
	v_mfma_f32_16x16x32_bf16 v[80:83], v[166:169], v[190:193], v[80:83]
	v_mfma_f32_16x16x32_bf16 v[120:123], v[100:103], v[198:201], v[120:123]
	v_mfma_f32_16x16x32_bf16 v[76:79], v[166:169], v[198:201], v[76:79]
	v_mfma_f32_16x16x32_bf16 v[132:135], v[104:107], v[178:181], v[132:135]
	v_mfma_f32_16x16x32_bf16 v[92:95], v[170:173], v[178:181], v[92:95]
	v_mfma_f32_16x16x32_bf16 v[128:131], v[104:107], v[186:189], v[128:131]
	v_mfma_f32_16x16x32_bf16 v[84:87], v[170:173], v[186:189], v[84:87]
	v_mfma_f32_16x16x32_bf16 v[124:127], v[104:107], v[194:197], v[124:127]
	v_mfma_f32_16x16x32_bf16 v[80:83], v[170:173], v[194:197], v[80:83]
	v_mfma_f32_16x16x32_bf16 v[120:123], v[104:107], v[202:205], v[120:123]
	v_mfma_f32_16x16x32_bf16 v[76:79], v[170:173], v[202:205], v[76:79]
	s_setprio 0
	s_barrier
; #define PG8_STAGE(bufoff, gbase, o0, o1) do { \
;         __builtin_amdgcn_global_load_lds((const unsigned*)((const char*)(gbase) + (o0)), (LAS unsigned*)(lds + (bufoff) + ldsw), 16, 0, 0); \
;         __builtin_amdgcn_global_load_lds((const unsigned*)((const char*)(gbase) + (o1)), (LAS unsigned*)(lds + (bufoff) + ldsw + 8192), 16, 0, 0); } while (0)
; #define PG8_LDA(dst, b, h) do { _Pragma("unroll") for (int m = 0; m < 4; ++m) _Pragma("unroll") for (int k = 0; k < 2; ++k) dst[m][k] = *(const LAS bf16x8*)(lds + PG8_SA(b, h) + aoff + m * 2048 + k * 1024); } while (0)
; #define PG8_WAIT_V(n) asm volatile("s_waitcnt vmcnt(" #n ")" ::: "memory")
; #define PG8_WAIT_L(n) asm volatile("s_waitcnt lgkmcnt(" #n ")" ::: "memory")
; #define PG8_BAR __builtin_amdgcn_s_barrier()
; #define PG8_SCHED __builtin_amdgcn_sched_barrier(0)
; template <class Epi, class Sched, class Prob>
; __device__ __forceinline__ void gemm_phase(LAS unsigned char* lds, LAS unsigned char* lds_epi, const Prob g, const Sched& S, const Epi& E, int wid) {
;     ...
;             PG8_LDA(At, 1, 1); PG8_STAGE(PG8_SB(1, 0), b3, vB0, vB1); PG8_STAGE(PG8_SB(1, 1), b3 + hstepB, vB0, vB1); PG8_STAGE(PG8_SA(1, 0), a3, cA00, cA01);
;             PG8_WAIT_V(8); PG8_WAIT_L(0); PG8_BAR; PG8_MMA(1, 0, At, B0); PG8_MMA(1, 1, At, B1); PG8_BAR; PG8_SCHED;
;         }
	s_mov_b32 m0, s31
	v_lshl_add_u64 v[206:207], v[206:207], 0, s[54:55]
	ds_read_b128 v[174:177], v223 offset:49152
	ds_read_b128 v[178:181], v223 offset:50176
	ds_read_b128 v[182:185], v223 offset:51200
	ds_read_b128 v[186:189], v223 offset:52224
	ds_read_b128 v[190:193], v223 offset:53248
	ds_read_b128 v[194:197], v223 offset:54272
	ds_read_b128 v[198:201], v223 offset:55296
	ds_read_b128 v[202:205], v223 offset:56320
	global_load_lds_dwordx4 v[206:207], off
	v_lshl_add_u64 v[206:207], v[208:209], 0, s[54:55]
	s_mov_b32 m0, s29
	s_nop 0
	global_load_lds_dwordx4 v[206:207], off
	v_lshl_add_u64 v[206:207], s[12:13], 0, v[152:153]
	s_mov_b32 m0, s30
	s_nop 0
	global_load_lds_dwordx4 v[206:207], off
	v_lshl_add_u64 v[206:207], s[12:13], 0, v[154:155]
	s_mov_b32 m0, s28
	s_nop 0
	global_load_lds_dwordx4 v[206:207], off
	v_lshl_add_u64 v[206:207], v[210:211], 0, s[54:55]
	s_mov_b32 m0, s83
	s_nop 0
	global_load_lds_dwordx4 v[206:207], off
	v_lshl_add_u64 v[206:207], v[212:213], 0, s[54:55]
	s_mov_b32 m0, s84
	s_nop 0
	global_load_lds_dwordx4 v[206:207], off
	s_waitcnt vmcnt(8)
	s_waitcnt lgkmcnt(0)
	s_barrier
	s_setprio 1
	s_waitcnt lgkmcnt(0)
	v_mfma_f32_16x16x32_bf16 v[64:67], v[56:59], v[174:177], v[64:67]
	v_mfma_f32_16x16x32_bf16 v[28:31], v[72:75], v[174:177], v[28:31]
	v_mfma_f32_16x16x32_bf16 v[60:63], v[56:59], v[182:185], v[60:63]
	v_mfma_f32_16x16x32_bf16 v[24:27], v[72:75], v[182:185], v[24:27]
	v_mfma_f32_16x16x32_bf16 v[52:55], v[56:59], v[190:193], v[52:55]
	v_mfma_f32_16x16x32_bf16 v[20:23], v[72:75], v[190:193], v[20:23]
	v_mfma_f32_16x16x32_bf16 v[48:51], v[56:59], v[198:201], v[48:51]
	v_mfma_f32_16x16x32_bf16 v[16:19], v[72:75], v[198:201], v[16:19]
	v_mfma_f32_16x16x32_bf16 v[64:67], v[68:71], v[178:181], v[64:67]
	v_mfma_f32_16x16x32_bf16 v[28:31], v[88:91], v[178:181], v[28:31]
	v_mfma_f32_16x16x32_bf16 v[60:63], v[68:71], v[186:189], v[60:63]
	v_mfma_f32_16x16x32_bf16 v[24:27], v[88:91], v[186:189], v[24:27]
	v_mfma_f32_16x16x32_bf16 v[52:55], v[68:71], v[194:197], v[52:55]
	v_mfma_f32_16x16x32_bf16 v[20:23], v[88:91], v[194:197], v[20:23]
	v_mfma_f32_16x16x32_bf16 v[48:51], v[68:71], v[202:205], v[48:51]
	v_mfma_f32_16x16x32_bf16 v[16:19], v[88:91], v[202:205], v[16:19]
	s_setprio 0
	s_setprio 1
	v_mfma_f32_16x16x32_bf16 v[44:47], v[100:103], v[174:177], v[44:47]
	v_mfma_f32_16x16x32_bf16 v[12:15], v[166:169], v[174:177], v[12:15]
	v_mfma_f32_16x16x32_bf16 v[40:43], v[100:103], v[182:185], v[40:43]
	v_mfma_f32_16x16x32_bf16 v[8:11], v[166:169], v[182:185], v[8:11]
	v_mfma_f32_16x16x32_bf16 v[36:39], v[100:103], v[190:193], v[36:39]
	v_mfma_f32_16x16x32_bf16 v[4:7], v[166:169], v[190:193], v[4:7]
	v_mfma_f32_16x16x32_bf16 v[32:35], v[100:103], v[198:201], v[32:35]
	v_mfma_f32_16x16x32_bf16 v[0:3], v[166:169], v[198:201], v[0:3]
	v_mfma_f32_16x16x32_bf16 v[44:47], v[104:107], v[178:181], v[44:47]
	v_mfma_f32_16x16x32_bf16 v[12:15], v[170:173], v[178:181], v[12:15]
	v_mfma_f32_16x16x32_bf16 v[40:43], v[104:107], v[186:189], v[40:43]
	v_mfma_f32_16x16x32_bf16 v[8:11], v[170:173], v[186:189], v[8:11]
	v_mfma_f32_16x16x32_bf16 v[36:39], v[104:107], v[194:197], v[36:39]
	v_mfma_f32_16x16x32_bf16 v[4:7], v[170:173], v[194:197], v[4:7]
	v_mfma_f32_16x16x32_bf16 v[32:35], v[104:107], v[202:205], v[32:35]
	v_mfma_f32_16x16x32_bf16 v[0:3], v[170:173], v[202:205], v[0:3]
	s_setprio 0
	s_barrier
	s_mov_b64 s[20:21], 0
	s_mov_b64 s[12:13], -1
	s_mov_b64 s[14:15], 0x100

; #define PG8_STAGE(bufoff, gbase, o0, o1) do { \
;         __builtin_amdgcn_global_load_lds((const unsigned*)((const char*)(gbase) + (o0)), (LAS unsigned*)(lds + (bufoff) + ldsw), 16, 0, 0); \
;         __builtin_amdgcn_global_load_lds((const unsigned*)((const char*)(gbase) + (o1)), (LAS unsigned*)(lds + (bufoff) + ldsw + 8192), 16, 0, 0); } while (0)
; #define PG8_LDA(dst, b, h) do { _Pragma("unroll") for (int m = 0; m < 4; ++m) _Pragma("unroll") for (int k = 0; k < 2; ++k) dst[m][k] = *(const LAS bf16x8*)(lds + PG8_SA(b, h) + aoff + m * 2048 + k * 1024); } while (0)
; #define PG8_LDB(dst, b, h) do { _Pragma("unroll") for (int n = 0; n < 2; ++n) _Pragma("unroll") for (int k = 0; k < 2; ++k) dst[n][k] = *(const LAS bf16x8*)(lds + PG8_SB(b, h) + boff + n * 2048 + k * 1024); } while (0)
; #define PG8_WAIT_V(n) asm volatile("s_waitcnt vmcnt(" #n ")" ::: "memory")
; #define PG8_WAIT_L(n) asm volatile("s_waitcnt lgkmcnt(" #n ")" ::: "memory")
; #define PG8_BAR __builtin_amdgcn_s_barrier()
; #define PG8_SCHED __builtin_amdgcn_sched_barrier(0)
; template <class Epi, class Sched, class Prob>
; __device__ __forceinline__ void gemm_phase(LAS unsigned char* lds, LAS unsigned char* lds_epi, const Prob g, const Sched& S, const Epi& E, int wid) {
;     ...
;         const bool has_next = S.next(ui + 1, nxt);
;         const char* nA = has_next ? g.a_base(nxt) : cA; const char* nB = has_next ? g.b_base(nxt) : cB;
; _Pragma("clang loop unroll(disable)")
;         for (int t = 0; t < nt; t += 2) {
;             const bool last = (t == nt - 2);
;             const char* a1 = cA + (size_t)(t + 1) * kstep;
;             const char* a2 = last ? nA : cA + (size_t)(t + 2) * kstep; const char* b2 = last ? nB : cB + (size_t)(t + 2) * kstep;
;             const char* a3 = a2 + kstep; const char* b3 = b2 + kstep;
;             PG8_LDB(B0, 0, 0); PG8_LDB(B1, 0, 1); PG8_SCHED; PG8_LDA(At, 0, 0); PG8_STAGE(PG8_SA(1, 1), a1, cA10, cA11);
;             PG8_WAIT_V(8); PG8_WAIT_L(0); PG8_BAR; PG8_MMA(0, 0, At, B0); PG8_MMA(0, 1, At, B1); PG8_BAR; PG8_SCHED;
;             PG8_LDA(At, 0, 1); PG8_STAGE(PG8_SB(0, 0), b2, vB0, vB1); PG8_STAGE(PG8_SB(0, 1), b2 + hstepB, vB0, vB1); PG8_STAGE(PG8_SA(0, 0), a2, cA00, cA01);
;             PG8_WAIT_V(8); PG8_WAIT_L(0); PG8_BAR; PG8_MMA(1, 0, At, B0); PG8_MMA(1, 1, At, B1); PG8_BAR; PG8_SCHED;
.LBB0_2090:
	s_ashr_i32 s11, s10, 31
	s_lshl_b64 s[30:31], s[10:11], 19
	s_add_u32 s30, s51, s30
	s_addc_u32 s31, s52, s31
	s_and_b64 s[40:41], s[40:41], exec
	s_cselect_b32 s11, s31, s37
	s_cselect_b32 s29, s30, s36
	s_add_u32 s36, s36, 0x80
	v_mov_b32_e32 v32, 0
	s_addc_u32 s37, s37, 0
	v_lshl_add_u64 v[182:183], v[0:1], 0, s[22:23]
	s_mov_b32 s69, -2
	ds_read_b128 v[24:27], v199
	ds_read_b128 v[28:31], v199 offset:1024
	ds_read_b128 v[16:19], v199 offset:2048
	ds_read_b128 v[20:23], v199 offset:3072
	ds_read_b128 v[8:11], v200
	ds_read_b128 v[12:15], v200 offset:1024
	ds_read_b128 v[0:3], v200 offset:2048
	ds_read_b128 v[4:7], v200 offset:3072
	s_add_u32 s40, s36, 0x80
	s_addc_u32 s41, s37, 0
	s_cmp_eq_u32 s69, 12
	s_cselect_b64 vcc, -1, 0
	s_cselect_b32 s41, s11, s41
	s_cselect_b32 s40, s29, s40
	v_cndmask_b32_e32 v185, v183, v181, vcc
	v_cndmask_b32_e32 v184, v182, v180, vcc
	v_lshl_add_u64 v[228:229], s[36:37], 0, v[176:177]
	s_add_i32 m0, s35, 0xc000
	ds_read_b128 v[186:189], v201
	ds_read_b128 v[190:193], v201 offset:1024
	ds_read_b128 v[204:207], v201 offset:2048
	ds_read_b128 v[208:211], v201 offset:3072
	ds_read_b128 v[212:215], v201 offset:4096
	ds_read_b128 v[216:219], v201 offset:5120
	ds_read_b128 v[220:223], v201 offset:6144
	ds_read_b128 v[224:227], v201 offset:7168
	global_load_lds_dwordx4 v[228:229], off
	v_lshl_add_u64 v[228:229], s[36:37], 0, v[174:175]
	s_add_i32 m0, s35, 0xe000
	s_nop 0
	global_load_lds_dwordx4 v[228:229], off
	s_waitcnt vmcnt(8)
	s_waitcnt lgkmcnt(0)
	s_barrier
	s_setprio 1
	s_waitcnt lgkmcnt(0)
	v_mfma_f32_16x16x128_f8f6f4 v[156:159], v[24:31], v[186:193], 0
	v_mfma_f32_16x16x128_f8f6f4 v[152:155], v[16:23], v[186:193], 0
	v_mfma_f32_16x16x128_f8f6f4 v[140:143], v[24:31], v[204:211], 0
	v_mfma_f32_16x16x128_f8f6f4 v[136:139], v[16:23], v[204:211], 0
	v_mfma_f32_16x16x128_f8f6f4 v[124:127], v[24:31], v[212:219], 0
	v_mfma_f32_16x16x128_f8f6f4 v[120:123], v[16:23], v[212:219], 0
	v_mfma_f32_16x16x128_f8f6f4 v[108:111], v[24:31], v[220:227], 0
	v_mfma_f32_16x16x128_f8f6f4 v[104:107], v[16:23], v[220:227], 0
	s_setprio 0
	s_setprio 1
	v_mfma_f32_16x16x128_f8f6f4 v[148:151], v[8:15], v[186:193], 0
	v_mfma_f32_16x16x128_f8f6f4 v[144:147], v[0:7], v[186:193], 0
	v_mfma_f32_16x16x128_f8f6f4 v[132:135], v[8:15], v[204:211], 0
	v_mfma_f32_16x16x128_f8f6f4 v[128:131], v[0:7], v[204:211], 0
	v_mfma_f32_16x16x128_f8f6f4 v[116:119], v[8:15], v[212:219], 0
	v_mfma_f32_16x16x128_f8f6f4 v[112:115], v[0:7], v[212:219], 0
	v_mfma_f32_16x16x128_f8f6f4 v[100:103], v[8:15], v[220:227], 0
	v_mfma_f32_16x16x128_f8f6f4 v[96:99], v[0:7], v[220:227], 0
	s_setprio 0
	s_barrier
	s_add_i32 s70, s63, s97
	v_lshl_add_u64 v[186:187], v[184:185], 0, v[160:161]
	s_mov_b32 m0, s70
	ds_read_b128 v[204:207], v201 offset:16384
	ds_read_b128 v[208:211], v201 offset:17408
	ds_read_b128 v[212:215], v201 offset:18432
	ds_read_b128 v[216:219], v201 offset:19456
	ds_read_b128 v[220:223], v201 offset:20480
	ds_read_b128 v[224:227], v201 offset:21504
	ds_read_b128 v[228:231], v201 offset:22528
	ds_read_b128 v[232:235], v201 offset:23552
	global_load_lds_dwordx4 v[186:187], off
	v_lshl_add_u64 v[188:189], v[184:185], 0, v[162:163]
	s_add_i32 m0, s70, 0x2000
	v_lshl_add_u64 v[190:191], v[184:185], 0, s[12:13]
	s_add_i32 s70, s64, s97
	global_load_lds_dwordx4 v[188:189], off
	v_lshl_add_u64 v[192:193], v[190:191], 0, v[160:161]
	s_mov_b32 m0, s70
	v_lshl_add_u64 v[190:191], v[190:191], 0, v[162:163]
	global_load_lds_dwordx4 v[192:193], off
	s_add_i32 m0, s70, 0x2000
	v_lshl_add_u64 v[192:193], s[40:41], 0, v[168:169]
	global_load_lds_dwordx4 v[190:191], off
	v_lshl_add_u64 v[190:191], s[40:41], 0, v[164:165]
	s_mov_b32 m0, s35
	s_nop 0
	global_load_lds_dwordx4 v[190:191], off
	s_mov_b32 m0, s58
	s_nop 0
	global_load_lds_dwordx4 v[192:193], off
	s_waitcnt vmcnt(8)
	s_waitcnt lgkmcnt(0)
	s_barrier
	s_setprio 1
	s_waitcnt lgkmcnt(0)
	v_mfma_f32_16x16x128_f8f6f4 v[92:95], v[24:31], v[204:211], 0
	v_mfma_f32_16x16x128_f8f6f4 v[88:91], v[16:23], v[204:211], 0
	v_mfma_f32_16x16x128_f8f6f4 v[76:79], v[24:31], v[212:219], 0
	v_mfma_f32_16x16x128_f8f6f4 v[72:75], v[16:23], v[212:219], 0
	v_mfma_f32_16x16x128_f8f6f4 v[60:63], v[24:31], v[220:227], 0
	v_mfma_f32_16x16x128_f8f6f4 v[56:59], v[16:23], v[220:227], 0
	v_mfma_f32_16x16x128_f8f6f4 v[44:47], v[24:31], v[228:235], 0
	v_mfma_f32_16x16x128_f8f6f4 v[40:43], v[16:23], v[228:235], 0
	s_setprio 0
	s_setprio 1
	v_mfma_f32_16x16x128_f8f6f4 v[84:87], v[8:15], v[204:211], 0
	v_mfma_f32_16x16x128_f8f6f4 v[80:83], v[0:7], v[204:211], 0
	v_mfma_f32_16x16x128_f8f6f4 v[68:71], v[8:15], v[212:219], 0
	v_mfma_f32_16x16x128_f8f6f4 v[64:67], v[0:7], v[212:219], 0
	v_mfma_f32_16x16x128_f8f6f4 v[52:55], v[8:15], v[220:227], 0
	v_mfma_f32_16x16x128_f8f6f4 v[48:51], v[0:7], v[220:227], 0
	v_mfma_f32_16x16x128_f8f6f4 v[36:39], v[8:15], v[228:235], 0
	v_mfma_f32_16x16x128_f8f6f4 v[32:35], v[0:7], v[228:235], 0
	s_setprio 0
	s_barrier
; #define PG8_STAGE(bufoff, gbase, o0, o1) do { \
;         __builtin_amdgcn_global_load_lds((const unsigned*)((const char*)(gbase) + (o0)), (LAS unsigned*)(lds + (bufoff) + ldsw), 16, 0, 0); \
;         __builtin_amdgcn_global_load_lds((const unsigned*)((const char*)(gbase) + (o1)), (LAS unsigned*)(lds + (bufoff) + ldsw + 8192), 16, 0, 0); } while (0)
; #define PG8_LDA(dst, b, h) do { _Pragma("unroll") for (int m = 0; m < 4; ++m) _Pragma("unroll") for (int k = 0; k < 2; ++k) dst[m][k] = *(const LAS bf16x8*)(lds + PG8_SA(b, h) + aoff + m * 2048 + k * 1024); } while (0)
; #define PG8_LDB(dst, b, h) do { _Pragma("unroll") for (int n = 0; n < 2; ++n) _Pragma("unroll") for (int k = 0; k < 2; ++k) dst[n][k] = *(const LAS bf16x8*)(lds + PG8_SB(b, h) + boff + n * 2048 + k * 1024); } while (0)
; #define PG8_WAIT_V(n) asm volatile("s_waitcnt vmcnt(" #n ")" ::: "memory")
; #define PG8_WAIT_L(n) asm volatile("s_waitcnt lgkmcnt(" #n ")" ::: "memory")
; #define PG8_BAR __builtin_amdgcn_s_barrier()
; #define PG8_SCHED __builtin_amdgcn_sched_barrier(0)
; template <class Epi, class Sched, class Prob>
; __device__ __forceinline__ void gemm_phase(LAS unsigned char* lds, LAS unsigned char* lds_epi, const Prob g, const Sched& S, const Epi& E, int wid) {
;     ...
;             PG8_LDB(B0, 1, 0); PG8_LDB(B1, 1, 1); PG8_SCHED; PG8_LDA(At, 1, 0); PG8_STAGE(PG8_SA(0, 1), a2, cA10, cA11);
;             PG8_WAIT_V(8); PG8_WAIT_L(0); PG8_BAR; PG8_MMA(0, 0, At, B0); PG8_MMA(0, 1, At, B1); PG8_BAR; PG8_SCHED;
;             PG8_LDA(At, 1, 1); PG8_STAGE(PG8_SB(1, 0), b3, vB0, vB1); PG8_STAGE(PG8_SB(1, 1), b3 + hstepB, vB0, vB1); PG8_STAGE(PG8_SA(1, 0), a3, cA00, cA01);
;             PG8_WAIT_V(8); PG8_WAIT_L(0); PG8_BAR; PG8_MMA(1, 0, At, B0); PG8_MMA(1, 1, At, B1); PG8_BAR; PG8_SCHED;
	s_add_i32 s70, 0, 0x18000
	s_add_i32 s71, 0, 0x1c000
	v_add_u32_e32 v12, s70, v195
	v_add_u32_e32 v28, s71, v195
	ds_read_b128 v[0:3], v12
	ds_read_b128 v[4:7], v12 offset:1024
	ds_read_b128 v[8:11], v12 offset:2048
	ds_read_b128 v[12:15], v12 offset:3072
	ds_read_b128 v[16:19], v28
	ds_read_b128 v[20:23], v28 offset:1024
	ds_read_b128 v[24:27], v28 offset:2048
	ds_read_b128 v[28:31], v28 offset:3072
	s_mov_b32 m0, s59
	v_lshl_add_u64 v[236:237], s[40:41], 0, v[166:167]
	ds_read_b128 v[204:207], v201 offset:32768
	ds_read_b128 v[208:211], v201 offset:33792
	ds_read_b128 v[212:215], v201 offset:34816
	ds_read_b128 v[216:219], v201 offset:35840
	ds_read_b128 v[220:223], v201 offset:36864
	ds_read_b128 v[224:227], v201 offset:37888
	ds_read_b128 v[228:231], v201 offset:38912
	ds_read_b128 v[232:235], v201 offset:39936
	global_load_lds_dwordx4 v[236:237], off
	v_lshl_add_u64 v[236:237], s[40:41], 0, v[170:171]
	s_mov_b32 m0, s60
	s_nop 0
	global_load_lds_dwordx4 v[236:237], off
	s_waitcnt vmcnt(8)
	s_waitcnt lgkmcnt(0)
	s_barrier
	s_setprio 1
	s_waitcnt lgkmcnt(0)
	v_mfma_f32_16x16x128_f8f6f4 v[156:159], v[0:7], v[204:211], v[156:159]
	v_mfma_f32_16x16x128_f8f6f4 v[152:155], v[8:15], v[204:211], v[152:155]
	v_mfma_f32_16x16x128_f8f6f4 v[140:143], v[0:7], v[212:219], v[140:143]
	v_mfma_f32_16x16x128_f8f6f4 v[136:139], v[8:15], v[212:219], v[136:139]
	v_mfma_f32_16x16x128_f8f6f4 v[124:127], v[0:7], v[220:227], v[124:127]
	v_mfma_f32_16x16x128_f8f6f4 v[120:123], v[8:15], v[220:227], v[120:123]
	v_mfma_f32_16x16x128_f8f6f4 v[108:111], v[0:7], v[228:235], v[108:111]
	v_mfma_f32_16x16x128_f8f6f4 v[104:107], v[8:15], v[228:235], v[104:107]
	s_setprio 0
	s_setprio 1
	v_mfma_f32_16x16x128_f8f6f4 v[148:151], v[16:23], v[204:211], v[148:151]
	v_mfma_f32_16x16x128_f8f6f4 v[144:147], v[24:31], v[204:211], v[144:147]
	v_mfma_f32_16x16x128_f8f6f4 v[132:135], v[16:23], v[212:219], v[132:135]
	v_mfma_f32_16x16x128_f8f6f4 v[128:131], v[24:31], v[212:219], v[128:131]
	v_mfma_f32_16x16x128_f8f6f4 v[116:119], v[16:23], v[220:227], v[116:119]
	v_mfma_f32_16x16x128_f8f6f4 v[112:115], v[24:31], v[220:227], v[112:115]
	v_mfma_f32_16x16x128_f8f6f4 v[100:103], v[16:23], v[228:235], v[100:103]
	v_mfma_f32_16x16x128_f8f6f4 v[96:99], v[24:31], v[228:235], v[96:99]
	s_setprio 0
	s_barrier
	s_add_i32 s40, s70, s97
	v_lshl_add_u64 v[186:187], v[186:187], 0, s[18:19]
	s_mov_b32 m0, s40
	ds_read_b128 v[204:207], v201 offset:49152
	ds_read_b128 v[208:211], v201 offset:50176
	ds_read_b128 v[212:215], v201 offset:51200
	ds_read_b128 v[216:219], v201 offset:52224
	ds_read_b128 v[220:223], v201 offset:53248
	ds_read_b128 v[224:227], v201 offset:54272
	ds_read_b128 v[228:231], v201 offset:55296
	ds_read_b128 v[232:235], v201 offset:56320
	global_load_lds_dwordx4 v[186:187], off
	v_lshl_add_u64 v[186:187], v[188:189], 0, s[18:19]
	s_add_i32 m0, s40, 0x2000
	v_lshl_add_u64 v[184:185], v[184:185], 0, s[20:21]
	s_add_i32 s40, s71, s97
	global_load_lds_dwordx4 v[186:187], off
	v_lshl_add_u64 v[186:187], v[184:185], 0, v[160:161]
	s_mov_b32 m0, s40
	v_lshl_add_u64 v[184:185], v[184:185], 0, v[162:163]
	global_load_lds_dwordx4 v[186:187], off
	s_add_i32 m0, s40, 0x2000
	s_nop 0
	global_load_lds_dwordx4 v[184:185], off
	v_lshl_add_u64 v[184:185], v[190:191], 0, s[18:19]
	s_mov_b32 m0, s61
	s_nop 0
	global_load_lds_dwordx4 v[184:185], off
	v_lshl_add_u64 v[184:185], v[192:193], 0, s[18:19]
	s_mov_b32 m0, s62
	s_nop 0
	global_load_lds_dwordx4 v[184:185], off
	s_waitcnt vmcnt(8)
	s_waitcnt lgkmcnt(0)
	s_barrier
	s_setprio 1
	s_waitcnt lgkmcnt(0)
	v_mfma_f32_16x16x128_f8f6f4 v[92:95], v[0:7], v[204:211], v[92:95]
	v_mfma_f32_16x16x128_f8f6f4 v[88:91], v[8:15], v[204:211], v[88:91]
	v_mfma_f32_16x16x128_f8f6f4 v[76:79], v[0:7], v[212:219], v[76:79]
	v_mfma_f32_16x16x128_f8f6f4 v[72:75], v[8:15], v[212:219], v[72:75]
	v_mfma_f32_16x16x128_f8f6f4 v[60:63], v[0:7], v[220:227], v[60:63]
	v_mfma_f32_16x16x128_f8f6f4 v[56:59], v[8:15], v[220:227], v[56:59]
	v_mfma_f32_16x16x128_f8f6f4 v[44:47], v[0:7], v[228:235], v[44:47]
	v_mfma_f32_16x16x128_f8f6f4 v[40:43], v[8:15], v[228:235], v[40:43]
	s_setprio 0
	s_setprio 1
	v_mfma_f32_16x16x128_f8f6f4 v[84:87], v[16:23], v[204:211], v[84:87]
	v_mfma_f32_16x16x128_f8f6f4 v[80:83], v[24:31], v[204:211], v[80:83]
	v_mfma_f32_16x16x128_f8f6f4 v[68:71], v[16:23], v[212:219], v[68:71]
	v_mfma_f32_16x16x128_f8f6f4 v[64:67], v[24:31], v[212:219], v[64:67]
	v_mfma_f32_16x16x128_f8f6f4 v[52:55], v[16:23], v[220:227], v[52:55]
	v_mfma_f32_16x16x128_f8f6f4 v[48:51], v[24:31], v[220:227], v[48:51]
	v_mfma_f32_16x16x128_f8f6f4 v[36:39], v[16:23], v[228:235], v[36:39]
	v_mfma_f32_16x16x128_f8f6f4 v[32:35], v[24:31], v[228:235], v[32:35]
	s_setprio 0
	s_barrier
	s_add_i32 s69, s69, 2
	s_add_u32 s36, s36, 0x100
	s_addc_u32 s37, s37, 0
	s_cmp_gt_u32 s69, 13
	v_lshl_add_u64 v[182:183], v[182:183], 0, s[22:23]

; #define PG8_STAGE(bufoff, gbase, o0, o1) do { \
;         __builtin_amdgcn_global_load_lds((const unsigned*)((const char*)(gbase) + (o0)), (LAS unsigned*)(lds + (bufoff) + ldsw), 16, 0, 0); \
;         __builtin_amdgcn_global_load_lds((const unsigned*)((const char*)(gbase) + (o1)), (LAS unsigned*)(lds + (bufoff) + ldsw + 8192), 16, 0, 0); } while (0)
; #define PG8_LDA(dst, b, h) do { _Pragma("unroll") for (int m = 0; m < 4; ++m) _Pragma("unroll") for (int k = 0; k < 2; ++k) dst[m][k] = *(const LAS bf16x8*)(lds + PG8_SA(b, h) + aoff + m * 2048 + k * 1024); } while (0)
; #define PG8_LDB(dst, b, h) do { _Pragma("unroll") for (int n = 0; n < 2; ++n) _Pragma("unroll") for (int k = 0; k < 2; ++k) dst[n][k] = *(const LAS bf16x8*)(lds + PG8_SB(b, h) + boff + n * 2048 + k * 1024); } while (0)
; #define PG8_WAIT_V(n) asm volatile("s_waitcnt vmcnt(" #n ")" ::: "memory")
; #define PG8_WAIT_L(n) asm volatile("s_waitcnt lgkmcnt(" #n ")" ::: "memory")
; #define PG8_BAR __builtin_amdgcn_s_barrier()
; #define PG8_SCHED __builtin_amdgcn_sched_barrier(0)
; template <class Epi, class Sched, class Prob>
; __device__ __forceinline__ void gemm_phase(LAS unsigned char* lds, LAS unsigned char* lds_epi, const Prob g, const Sched& S, const Epi& E, int wid) {
;     ...
;         const bool has_next = S.next(ui + 1, nxt);
;         const char* nA = has_next ? g.a_base(nxt) : cA; const char* nB = has_next ? g.b_base(nxt) : cB;
; _Pragma("clang loop unroll(disable)")
;         for (int t = 0; t < nt; t += 2) {
;             const bool last = (t == nt - 2);
;             const char* a1 = cA + (size_t)(t + 1) * kstep;
;             const char* a2 = last ? nA : cA + (size_t)(t + 2) * kstep; const char* b2 = last ? nB : cB + (size_t)(t + 2) * kstep;
;             const char* a3 = a2 + kstep; const char* b3 = b2 + kstep;
;             PG8_LDB(B0, 0, 0); PG8_LDB(B1, 0, 1); PG8_SCHED; PG8_LDA(At, 0, 0); PG8_STAGE(PG8_SA(1, 1), a1, cA10, cA11);
;             PG8_WAIT_V(8); PG8_WAIT_L(0); PG8_BAR; PG8_MMA(0, 0, At, B0); PG8_MMA(0, 1, At, B1); PG8_BAR; PG8_SCHED;
;             PG8_LDA(At, 0, 1); PG8_STAGE(PG8_SB(0, 0), b2, vB0, vB1); PG8_STAGE(PG8_SB(0, 1), b2 + hstepB, vB0, vB1); PG8_STAGE(PG8_SA(0, 0), a2, cA00, cA01);
;             PG8_WAIT_V(8); PG8_WAIT_L(0); PG8_BAR; PG8_MMA(1, 0, At, B0); PG8_MMA(1, 1, At, B1); PG8_BAR; PG8_SCHED;
.LBB0_2172:
	s_add_u32 s36, s36, 0x80
	v_mov_b32_e32 v32, 0
	s_addc_u32 s37, s37, 0
	v_lshl_add_u64 v[186:187], v[0:1], 0, s[22:23]
	s_mov_b32 s64, -2
	ds_read_b128 v[24:27], v161
	ds_read_b128 v[28:31], v161 offset:1024
	ds_read_b128 v[16:19], v161 offset:2048
	ds_read_b128 v[20:23], v161 offset:3072
	ds_read_b128 v[8:11], v207
	ds_read_b128 v[12:15], v207 offset:1024
	ds_read_b128 v[0:3], v207 offset:2048
	ds_read_b128 v[4:7], v207 offset:3072
	s_add_u32 s40, s36, 0x80
	s_addc_u32 s41, s37, 0
	s_cmp_eq_u32 s64, 52
	s_cselect_b64 vcc, -1, 0
	s_cselect_b32 s41, s31, s41
	s_cselect_b32 s40, s30, s40
	v_cndmask_b32_e32 v189, v187, v185, vcc
	v_cndmask_b32_e32 v188, v186, v184, vcc
	v_lshl_add_u64 v[212:213], s[36:37], 0, v[182:183]
	s_add_i32 m0, s33, 0xc000
	ds_read_b128 v[190:193], v208
	ds_read_b128 v[194:197], v208 offset:1024
	ds_read_b128 v[216:219], v208 offset:2048
	ds_read_b128 v[220:223], v208 offset:3072
	ds_read_b128 v[224:227], v208 offset:4096
	ds_read_b128 v[228:231], v208 offset:5120
	ds_read_b128 v[238:241], v208 offset:6144
	ds_read_b128 v[242:245], v208 offset:7168
	global_load_lds_dwordx4 v[212:213], off
	v_lshl_add_u64 v[212:213], s[36:37], 0, v[180:181]
	s_add_i32 m0, s33, 0xe000
	s_nop 0
	global_load_lds_dwordx4 v[212:213], off
	s_waitcnt vmcnt(8)
	s_waitcnt lgkmcnt(0)
	s_barrier
	s_setprio 1
	s_waitcnt lgkmcnt(0)
	v_mfma_f32_16x16x128_f8f6f4 v[156:159], v[24:31], v[190:197], 0
	v_mfma_f32_16x16x128_f8f6f4 v[152:155], v[16:23], v[190:197], 0
	v_mfma_f32_16x16x128_f8f6f4 v[140:143], v[24:31], v[216:223], 0
	v_mfma_f32_16x16x128_f8f6f4 v[136:139], v[16:23], v[216:223], 0
	v_mfma_f32_16x16x128_f8f6f4 v[124:127], v[24:31], v[224:231], 0
	v_mfma_f32_16x16x128_f8f6f4 v[120:123], v[16:23], v[224:231], 0
	v_mfma_f32_16x16x128_f8f6f4 v[108:111], v[24:31], v[238:245], 0
	v_mfma_f32_16x16x128_f8f6f4 v[104:107], v[16:23], v[238:245], 0
	s_setprio 0
	s_setprio 1
	v_mfma_f32_16x16x128_f8f6f4 v[148:151], v[8:15], v[190:197], 0
	v_mfma_f32_16x16x128_f8f6f4 v[144:147], v[0:7], v[190:197], 0
	v_mfma_f32_16x16x128_f8f6f4 v[132:135], v[8:15], v[216:223], 0
	v_mfma_f32_16x16x128_f8f6f4 v[128:131], v[0:7], v[216:223], 0
	v_mfma_f32_16x16x128_f8f6f4 v[116:119], v[8:15], v[224:231], 0
	v_mfma_f32_16x16x128_f8f6f4 v[112:115], v[0:7], v[224:231], 0
	v_mfma_f32_16x16x128_f8f6f4 v[100:103], v[8:15], v[238:245], 0
	v_mfma_f32_16x16x128_f8f6f4 v[96:99], v[0:7], v[238:245], 0
	s_setprio 0
	s_barrier
	s_add_i32 s65, s58, s97
	v_lshl_add_u64 v[190:191], v[188:189], 0, v[162:163]
	s_mov_b32 m0, s65
	ds_read_b128 v[216:219], v208 offset:16384
	ds_read_b128 v[220:223], v208 offset:17408
	ds_read_b128 v[224:227], v208 offset:18432
	ds_read_b128 v[228:231], v208 offset:19456
	ds_read_b128 v[238:241], v208 offset:20480
	ds_read_b128 v[242:245], v208 offset:21504
	ds_read_b128 v[246:249], v208 offset:22528
	ds_read_b128 v[250:253], v208 offset:23552
	global_load_lds_dwordx4 v[190:191], off
	v_lshl_add_u64 v[192:193], v[188:189], 0, v[164:165]
	s_add_i32 m0, s65, 0x2000
	v_lshl_add_u64 v[194:195], v[188:189], 0, s[16:17]
	s_add_i32 s65, s59, s97
	global_load_lds_dwordx4 v[192:193], off
	v_lshl_add_u64 v[196:197], v[194:195], 0, v[162:163]
	s_mov_b32 m0, s65
	v_lshl_add_u64 v[194:195], v[194:195], 0, v[164:165]
	global_load_lds_dwordx4 v[196:197], off
	s_add_i32 m0, s65, 0x2000
	v_lshl_add_u64 v[196:197], s[40:41], 0, v[174:175]
	global_load_lds_dwordx4 v[194:195], off
	v_lshl_add_u64 v[194:195], s[40:41], 0, v[170:171]
	s_mov_b32 m0, s33
	s_nop 0
	global_load_lds_dwordx4 v[194:195], off
	s_mov_b32 m0, s35
	s_nop 0
	global_load_lds_dwordx4 v[196:197], off
	s_waitcnt vmcnt(8)
	s_waitcnt lgkmcnt(0)
	s_barrier
	s_setprio 1
	s_waitcnt lgkmcnt(0)
	v_mfma_f32_16x16x128_f8f6f4 v[92:95], v[24:31], v[216:223], 0
	v_mfma_f32_16x16x128_f8f6f4 v[88:91], v[16:23], v[216:223], 0
	v_mfma_f32_16x16x128_f8f6f4 v[76:79], v[24:31], v[224:231], 0
	v_mfma_f32_16x16x128_f8f6f4 v[72:75], v[16:23], v[224:231], 0
	v_mfma_f32_16x16x128_f8f6f4 v[60:63], v[24:31], v[238:245], 0
	v_mfma_f32_16x16x128_f8f6f4 v[56:59], v[16:23], v[238:245], 0
	v_mfma_f32_16x16x128_f8f6f4 v[44:47], v[24:31], v[246:253], 0
	v_mfma_f32_16x16x128_f8f6f4 v[40:43], v[16:23], v[246:253], 0
	s_setprio 0
	s_setprio 1
	v_mfma_f32_16x16x128_f8f6f4 v[84:87], v[8:15], v[216:223], 0
	v_mfma_f32_16x16x128_f8f6f4 v[80:83], v[0:7], v[216:223], 0
	v_mfma_f32_16x16x128_f8f6f4 v[68:71], v[8:15], v[224:231], 0
	v_mfma_f32_16x16x128_f8f6f4 v[64:67], v[0:7], v[224:231], 0
	v_mfma_f32_16x16x128_f8f6f4 v[52:55], v[8:15], v[238:245], 0
	v_mfma_f32_16x16x128_f8f6f4 v[48:51], v[0:7], v[238:245], 0
	v_mfma_f32_16x16x128_f8f6f4 v[36:39], v[8:15], v[246:253], 0
	v_mfma_f32_16x16x128_f8f6f4 v[32:35], v[0:7], v[246:253], 0
	s_setprio 0
	s_barrier
; #define PG8_STAGE(bufoff, gbase, o0, o1) do { \
;         __builtin_amdgcn_global_load_lds((const unsigned*)((const char*)(gbase) + (o0)), (LAS unsigned*)(lds + (bufoff) + ldsw), 16, 0, 0); \
;         __builtin_amdgcn_global_load_lds((const unsigned*)((const char*)(gbase) + (o1)), (LAS unsigned*)(lds + (bufoff) + ldsw + 8192), 16, 0, 0); } while (0)
; #define PG8_LDA(dst, b, h) do { _Pragma("unroll") for (int m = 0; m < 4; ++m) _Pragma("unroll") for (int k = 0; k < 2; ++k) dst[m][k] = *(const LAS bf16x8*)(lds + PG8_SA(b, h) + aoff + m * 2048 + k * 1024); } while (0)
; #define PG8_LDB(dst, b, h) do { _Pragma("unroll") for (int n = 0; n < 2; ++n) _Pragma("unroll") for (int k = 0; k < 2; ++k) dst[n][k] = *(const LAS bf16x8*)(lds + PG8_SB(b, h) + boff + n * 2048 + k * 1024); } while (0)
; #define PG8_WAIT_V(n) asm volatile("s_waitcnt vmcnt(" #n ")" ::: "memory")
; #define PG8_WAIT_L(n) asm volatile("s_waitcnt lgkmcnt(" #n ")" ::: "memory")
; #define PG8_BAR __builtin_amdgcn_s_barrier()
; #define PG8_SCHED __builtin_amdgcn_sched_barrier(0)
; template <class Epi, class Sched, class Prob>
; __device__ __forceinline__ void gemm_phase(LAS unsigned char* lds, LAS unsigned char* lds_epi, const Prob g, const Sched& S, const Epi& E, int wid) {
;     ...
;             PG8_LDB(B0, 1, 0); PG8_LDB(B1, 1, 1); PG8_SCHED; PG8_LDA(At, 1, 0); PG8_STAGE(PG8_SA(0, 1), a2, cA10, cA11);
;             PG8_WAIT_V(8); PG8_WAIT_L(0); PG8_BAR; PG8_MMA(0, 0, At, B0); PG8_MMA(0, 1, At, B1); PG8_BAR; PG8_SCHED;
;             PG8_LDA(At, 1, 1); PG8_STAGE(PG8_SB(1, 0), b3, vB0, vB1); PG8_STAGE(PG8_SB(1, 1), b3 + hstepB, vB0, vB1); PG8_STAGE(PG8_SA(1, 0), a3, cA00, cA01);
;             PG8_WAIT_V(8); PG8_WAIT_L(0); PG8_BAR; PG8_MMA(1, 0, At, B0); PG8_MMA(1, 1, At, B1); PG8_BAR; PG8_SCHED;
	s_add_i32 s65, 0, 0x18000
	s_add_i32 s66, 0, 0x1c000
	v_add_u32_e32 v12, s65, v204
	v_add_u32_e32 v28, s66, v204
	ds_read_b128 v[0:3], v12
	ds_read_b128 v[4:7], v12 offset:1024
	ds_read_b128 v[8:11], v12 offset:2048
	ds_read_b128 v[12:15], v12 offset:3072
	ds_read_b128 v[16:19], v28
	ds_read_b128 v[20:23], v28 offset:1024
	ds_read_b128 v[24:27], v28 offset:2048
	ds_read_b128 v[28:31], v28 offset:3072
	s_mov_b32 m0, s48
	v_lshl_add_u64 v[212:213], s[40:41], 0, v[172:173]
	ds_read_b128 v[216:219], v208 offset:32768
	ds_read_b128 v[220:223], v208 offset:33792
	ds_read_b128 v[224:227], v208 offset:34816
	ds_read_b128 v[228:231], v208 offset:35840
	ds_read_b128 v[238:241], v208 offset:36864
	ds_read_b128 v[242:245], v208 offset:37888
	ds_read_b128 v[246:249], v208 offset:38912
	ds_read_b128 v[250:253], v208 offset:39936
	global_load_lds_dwordx4 v[212:213], off
	v_lshl_add_u64 v[212:213], s[40:41], 0, v[176:177]
	s_mov_b32 m0, s52
	s_nop 0
	global_load_lds_dwordx4 v[212:213], off
	s_waitcnt vmcnt(8)
	s_waitcnt lgkmcnt(0)
	s_barrier
	s_setprio 1
	s_waitcnt lgkmcnt(0)
	v_mfma_f32_16x16x128_f8f6f4 v[156:159], v[0:7], v[216:223], v[156:159]
	v_mfma_f32_16x16x128_f8f6f4 v[152:155], v[8:15], v[216:223], v[152:155]
	v_mfma_f32_16x16x128_f8f6f4 v[140:143], v[0:7], v[224:231], v[140:143]
	v_mfma_f32_16x16x128_f8f6f4 v[136:139], v[8:15], v[224:231], v[136:139]
	v_mfma_f32_16x16x128_f8f6f4 v[124:127], v[0:7], v[238:245], v[124:127]
	v_mfma_f32_16x16x128_f8f6f4 v[120:123], v[8:15], v[238:245], v[120:123]
	v_mfma_f32_16x16x128_f8f6f4 v[108:111], v[0:7], v[246:253], v[108:111]
	v_mfma_f32_16x16x128_f8f6f4 v[104:107], v[8:15], v[246:253], v[104:107]
	s_setprio 0
	s_setprio 1
	v_mfma_f32_16x16x128_f8f6f4 v[148:151], v[16:23], v[216:223], v[148:151]
	v_mfma_f32_16x16x128_f8f6f4 v[144:147], v[24:31], v[216:223], v[144:147]
	v_mfma_f32_16x16x128_f8f6f4 v[132:135], v[16:23], v[224:231], v[132:135]
	v_mfma_f32_16x16x128_f8f6f4 v[128:131], v[24:31], v[224:231], v[128:131]
	v_mfma_f32_16x16x128_f8f6f4 v[116:119], v[16:23], v[238:245], v[116:119]
	v_mfma_f32_16x16x128_f8f6f4 v[112:115], v[24:31], v[238:245], v[112:115]
	v_mfma_f32_16x16x128_f8f6f4 v[100:103], v[16:23], v[246:253], v[100:103]
	v_mfma_f32_16x16x128_f8f6f4 v[96:99], v[24:31], v[246:253], v[96:99]
	s_setprio 0
	s_barrier
	s_add_i32 s40, s65, s97
	v_lshl_add_u64 v[190:191], v[190:191], 0, s[18:19]
	s_mov_b32 m0, s40
	ds_read_b128 v[216:219], v208 offset:49152
	ds_read_b128 v[220:223], v208 offset:50176
	ds_read_b128 v[224:227], v208 offset:51200
	ds_read_b128 v[228:231], v208 offset:52224
	ds_read_b128 v[238:241], v208 offset:53248
	ds_read_b128 v[242:245], v208 offset:54272
	ds_read_b128 v[246:249], v208 offset:55296
	ds_read_b128 v[250:253], v208 offset:56320
	global_load_lds_dwordx4 v[190:191], off
	v_lshl_add_u64 v[190:191], v[192:193], 0, s[18:19]
	s_add_i32 m0, s40, 0x2000
	v_lshl_add_u64 v[188:189], v[188:189], 0, s[20:21]
	s_add_i32 s40, s66, s97
	global_load_lds_dwordx4 v[190:191], off
	v_lshl_add_u64 v[190:191], v[188:189], 0, v[162:163]
	s_mov_b32 m0, s40
	v_lshl_add_u64 v[188:189], v[188:189], 0, v[164:165]
	global_load_lds_dwordx4 v[190:191], off
	s_add_i32 m0, s40, 0x2000
	s_nop 0
	global_load_lds_dwordx4 v[188:189], off
	v_lshl_add_u64 v[188:189], v[194:195], 0, s[18:19]
	s_mov_b32 m0, s54
	s_nop 0
	global_load_lds_dwordx4 v[188:189], off
	v_lshl_add_u64 v[188:189], v[196:197], 0, s[18:19]
	s_mov_b32 m0, s55
	s_nop 0
	global_load_lds_dwordx4 v[188:189], off
	s_waitcnt vmcnt(8)
	s_waitcnt lgkmcnt(0)
	s_barrier
	s_setprio 1
	s_waitcnt lgkmcnt(0)
	v_mfma_f32_16x16x128_f8f6f4 v[92:95], v[0:7], v[216:223], v[92:95]
	v_mfma_f32_16x16x128_f8f6f4 v[88:91], v[8:15], v[216:223], v[88:91]
	v_mfma_f32_16x16x128_f8f6f4 v[76:79], v[0:7], v[224:231], v[76:79]
	v_mfma_f32_16x16x128_f8f6f4 v[72:75], v[8:15], v[224:231], v[72:75]
	v_mfma_f32_16x16x128_f8f6f4 v[60:63], v[0:7], v[238:245], v[60:63]
	v_mfma_f32_16x16x128_f8f6f4 v[56:59], v[8:15], v[238:245], v[56:59]
	v_mfma_f32_16x16x128_f8f6f4 v[44:47], v[0:7], v[246:253], v[44:47]
	v_mfma_f32_16x16x128_f8f6f4 v[40:43], v[8:15], v[246:253], v[40:43]
	s_setprio 0
	s_setprio 1
	v_mfma_f32_16x16x128_f8f6f4 v[84:87], v[16:23], v[216:223], v[84:87]
	v_mfma_f32_16x16x128_f8f6f4 v[80:83], v[24:31], v[216:223], v[80:83]
	v_mfma_f32_16x16x128_f8f6f4 v[68:71], v[16:23], v[224:231], v[68:71]
	v_mfma_f32_16x16x128_f8f6f4 v[64:67], v[24:31], v[224:231], v[64:67]
	v_mfma_f32_16x16x128_f8f6f4 v[52:55], v[16:23], v[238:245], v[52:55]
	v_mfma_f32_16x16x128_f8f6f4 v[48:51], v[24:31], v[238:245], v[48:51]
	v_mfma_f32_16x16x128_f8f6f4 v[36:39], v[16:23], v[246:253], v[36:39]
	v_mfma_f32_16x16x128_f8f6f4 v[32:35], v[24:31], v[246:253], v[32:35]
	s_setprio 0
	s_barrier
	s_add_i32 s64, s64, 2
	s_add_u32 s36, s36, 0x100
	s_addc_u32 s37, s37, 0
	s_cmp_gt_u32 s64, 53
	v_lshl_add_u64 v[186:187], v[186:187], 0, s[22:23]
